# router tails: xor-4 transposing exchange via two bank-masked DPP moves; layer-1 key-pass 16-lane sum via DPP (on top of v87)
# baseline (speedup 1.0000x reference)
; __device__ __forceinline__ float bflo(unsigned w) { return __uint_as_float(w << 16); }
; __device__ __forceinline__ float bfhi(unsigned w) { return __uint_as_float(w & 0xffff0000u); }
; __device__ __forceinline__ void phase_qkfix(const Params& p, const Ctx& F, const int l) {
;     ...
;     for (long V0 = (long)F.gw * 4; V0 < total; V0 += (long)F.NGW * 4) {
;         const long V = V0 + sub; const bool valid = V < total; const long Vc = valid ? V : 0;
;         const int rr = (int)(Vc / NV), v = (int)(Vc % NV);
;         int R, pos; bool lat;
;         if (l == 0) { const int b = rr >> 12, s = rr & 4095; R = b * TPB + CTXL + s; pos = s; lat = true; }
;         else { R = rr; const int t = rr % TPB; lat = t >= CTXL; pos = t - CTXL; }
;         const int col = l == 0 ? v * 128 + (v >= 10 ? 256 : 0) : (8 + v) * 128;
;         bf16_t* ptr = F.r2 + (size_t)R * INW + col + ax * 64 + f0;
;         const u32x2 wl = *(const u32x2*)ptr, wh = *(const u32x2*)(ptr + 32);
;         float xl[4] = {bflo(wl.x), bfhi(wl.x), bflo(wl.y), bfhi(wl.y)}, xh[4] = {bflo(wh.x), bfhi(wh.x), bflo(wh.y), bfhi(wh.y)};
;         if (l == 1) {
;             float ss = 0.f;
; #pragma unroll
;             for (int q = 0; q < 4; ++q) ss += xl[q] * xl[q] + xh[q] * xh[q];
;             ss += __shfl_xor(ss, 1); ss += __shfl_xor(ss, 2); ss += __shfl_xor(ss, 4); ss += __shfl_xor(ss, 8);
;             const float rstd = rsqrtf(ss * (1.f / 128.f) + EPS);
;             const float* g = p.kn + ax * 64 + f0;
; #pragma unroll
;             for (int q = 0; q < 4; ++q) { xl[q] = xl[q] * rstd * g[q]; xh[q] = xh[q] * rstd * g[32 + q]; }
;         }
;         if (lat) {
;             const int pp = ax == 0 ? (pos >> 6) : (pos & 63);
; #pragma unroll
;             for (int q = 0; q < 4; ++q) { const f32x2 c = cs[pp * 32 + f0 + q]; const float a = xl[q], bq = xh[q]; xl[q] = a * c.x - bq * c.y; xh[q] = bq * c.x + a * c.y; }
.LBB0_444:
	v_lshl_add_u64 v[20:21], v[10:11], 0, s[2:3]
	s_mov_b64 s[4:5], 0x11000
	v_cmp_gt_i64_e32 vcc, s[4:5], v[20:21]
	v_mov_b32_e32 v19, v35
	v_mov_b32_e32 v15, v35
	v_cndmask_b32_e32 v23, 0, v21, vcc
	v_cndmask_b32_e32 v22, 0, v20, vcc
	v_lshrrev_b32_e32 v34, 31, v23
	v_lshl_add_u64 v[24:25], v[22:23], 0, v[34:35]
	v_and_b32_e32 v1, -2, v24
	v_sub_co_u32_e64 v9, s[4:5], v22, v1
	v_ashrrev_i64 v[20:21], 1, v[24:25]
	s_nop 0
	v_subb_co_u32_e64 v5, s[4:5], v23, v25, s[4:5]
	v_mov_b32_e32 v1, 0x400
	v_mov_b64_e32 v[22:23], s[66:67]
	v_lshl_add_u32 v34, v9, 7, v1
	v_mad_i64_i32 v[22:23], s[4:5], v20, s92, v[22:23]
	v_lshl_add_u64 v[22:23], v[34:35], 1, v[22:23]
	v_lshl_add_u64 v[22:23], v[22:23], 0, v[18:19]
	v_lshl_add_u64 v[22:23], v[22:23], 0, v[14:15]
	global_load_dwordx2 v[24:25], v[22:23], off
	s_nop 0
	global_load_dwordx2 v[22:23], v[22:23], off offset:64
	s_mov_b32 s4, 0x78787879
	v_mul_hi_i32 v19, v20, s4
	v_lshrrev_b32_e32 v21, 31, v19
	v_ashrrev_i32_e32 v19, 11, v19
	v_add_u32_e32 v19, v19, v21
	s_movk_i32 s6, 0xff
	s_waitcnt vmcnt(1)
	v_lshlrev_b32_e32 v27, 16, v25
	v_and_b32_e32 v31, 0xffff0000, v25
	s_waitcnt vmcnt(0)
	v_and_b32_e32 v30, 0xffff0000, v23
	v_lshlrev_b32_e32 v40, 16, v24
	v_and_b32_e32 v41, 0xffff0000, v24
	v_lshlrev_b32_e32 v24, 16, v22
	v_and_b32_e32 v25, 0xffff0000, v22
	v_lshlrev_b32_e32 v29, 16, v23
	v_mov_b32_e32 v28, v30
	v_pk_mul_f32 v[22:23], v[24:25], v[24:25]
	v_mov_b32_e32 v26, v31
	v_pk_mul_f32 v[42:43], v[28:29], v[28:29]
	v_pk_fma_f32 v[22:23], v[40:41], v[40:41], v[22:23]
	v_pk_fma_f32 v[42:43], v[26:27], v[26:27], v[42:43]
	v_add_f32_e32 v1, v22, v23
	v_add_f32_e32 v1, v43, v1
	v_add_f32_e32 v1, v42, v1
	s_nop 1
	v_add_f32_dpp v1, v1, v1 quad_perm:[1,0,3,2] row_mask:0xf bank_mask:0xf
	s_nop 1
	v_add_f32_dpp v1, v1, v1 quad_perm:[2,3,0,1] row_mask:0xf bank_mask:0xf
	s_nop 1
	v_add_f32_dpp v1, v1, v1 row_half_mirror row_mask:0xf bank_mask:0xf
	s_nop 1
	v_add_f32_dpp v1, v1, v1 row_mirror row_mask:0xf bank_mask:0xf
	v_fmamk_f32 v1, v1, 0x3c000000, v196
	v_mul_f32_e32 v15, 0x4b800000, v1
	v_cmp_gt_f32_e64 s[4:5], s52, v1
	s_nop 1
	v_cndmask_b32_e64 v1, v1, v15, s[4:5]
	v_rsq_f32_e32 v1, v1
	v_mul_i32_i24_e32 v15, 0x1100, v19
	v_sub_u32_e32 v15, v20, v15
	v_cmp_lt_i32_e64 s[6:7], s6, v15
	v_mul_f32_e32 v19, 0x45800000, v1
	v_cndmask_b32_e64 v22, v1, v19, s[4:5]
	v_pk_mul_f32 v[40:41], v[22:23], v[40:41] op_sel_hi:[0,1]
	v_pk_mul_f32 v[42:43], v[22:23], v[24:25] op_sel_hi:[0,1]
	v_mul_f32_e32 v1, v22, v27
	v_mul_f32_e32 v19, v22, v29
	v_pk_mul_f32 v[30:31], v[22:23], v[30:31] op_sel_hi:[0,1]
	v_pk_mul_f32 v[24:25], v[2:3], v[40:41]
	v_pk_mul_f32 v[22:23], v[6:7], v[42:43]
	v_mul_f32_e32 v26, v4, v1
	v_mul_f32_e32 v28, v8, v19
	v_pk_mul_f32 v[30:31], v[16:17], v[30:31]
	s_and_saveexec_b64 s[4:5], s[6:7]
	s_cbranch_execz .LBB0_446
	v_add_u32_e32 v1, 0x3fffff00, v15
	v_lshrrev_b32_e32 v1, 6, v1
	v_and_b32_e32 v15, 63, v15
	v_cndmask_b32_e64 v1, v15, v1, s[0:1]
	v_lshl_add_u32 v1, v1, 8, v33
	ds_read_b128 v[40:43], v1
	ds_read_b128 v[44:47], v1 offset:16
	s_waitcnt lgkmcnt(1)
	v_mov_b32_e32 v49, v42
	s_waitcnt lgkmcnt(0)
	v_mul_f32_e32 v50, v26, v44
	v_mul_f32_e32 v52, v28, v45
	v_mul_f32_e32 v28, v28, v44
	v_mul_f32_e32 v44, v26, v45
	v_pk_mul_f32 v[26:27], v[30:31], v[46:47] op_sel:[1,0] op_sel_hi:[0,1]
	v_pk_mul_f32 v[30:31], v[30:31], v[46:47]
	v_mov_b32_e32 v42, v41
	v_mov_b32_e32 v51, v26
	v_mov_b32_e32 v53, v27
	v_mov_b32_e32 v29, v30
	v_mov_b32_e32 v45, v31
	v_mov_b32_e32 v48, v40
	v_pk_mul_f32 v[40:41], v[22:23], v[42:43]
	v_pk_mul_f32 v[42:43], v[24:25], v[42:43]
	v_pk_add_f32 v[26:27], v[50:51], v[52:53] neg_lo:[0,1] neg_hi:[0,1]
	v_pk_add_f32 v[28:29], v[28:29], v[44:45]
	v_pk_fma_f32 v[24:25], v[24:25], v[48:49], v[40:41] neg_lo:[0,0,1] neg_hi:[0,0,1]
	v_pk_fma_f32 v[22:23], v[22:23], v[48:49], v[42:43]
	v_mov_b32_e32 v30, v29
	v_mov_b32_e32 v31, v27

; #define LAS __attribute__((address_space(3)))
; __device__ __forceinline__ void phase_norm2(const Params& p, const Ctx& F, const int l) {
;     ...
;         if (F.lane == 0) { F.sah[b * TPB + t] = am0 * (1.f / 127.f); if (two) F.sah[b * TPB + tB] = am1 * (1.f / 127.f); }
;         f32x2 lg[16];
;         unsigned wro = (unsigned)(uintptr_t)wr; asm volatile("" : "+v"(wro));
;         const LAS float* wr2 = (const LAS float*)(uintptr_t)wro;
; #pragma unroll
;         for (int e = 0; e < 16; ++e) { f32x2 a = {0.f, 0.f};
; #pragma unroll
;             for (int j = 0; j < 8; ++j) { const f32x4 w = *((const LAS f32x4*)(wr2 + e * DM) + F.lane + 64 * j);
; #pragma unroll
;                 for (int c = 0; c < 4; ++c) a += vv[j][c] * w[c]; }
;             lg[e] = a; }
.LBB0_937:
	s_or_b64 exec, exec, s[12:13]
	v_mov_b32_e32 v1, v35
	s_nop 0
	v_lshl_add_u32 v182, v132, 4, v1
	v_add_u32_e32 v244, 0x10000, v182
	ds_read_b128 v[224:227], v182
	ds_read_b128 v[228:231], v182 offset:1024
	ds_read_b128 v[232:235], v182 offset:2048
	ds_read_b128 v[236:239], v182 offset:3072
	s_waitcnt lgkmcnt(3)
	v_pk_fma_f32 v[156:157], v[124:125], v[224:225], 0 op_sel_hi:[1,0,0]
	s_nop 0
	v_pk_fma_f32 v[152:153], v[126:127], v[224:225], v[156:157] op_sel:[0,1,0]
	s_nop 0
	v_pk_fma_f32 v[152:153], v[128:129], v[226:227], v[152:153] op_sel_hi:[1,0,1]
	v_mov_b32_e32 v154, v227
	v_pk_fma_f32 v[156:157], v[130:131], v[154:155], v[152:153] op_sel_hi:[1,0,1]
	ds_read_b128 v[240:243], v182 offset:4096
	s_waitcnt lgkmcnt(3)
	v_pk_fma_f32 v[156:157], v[112:113], v[228:229], v[156:157] op_sel_hi:[1,0,1]
	s_nop 0
	v_pk_fma_f32 v[152:153], v[114:115], v[228:229], v[156:157] op_sel:[0,1,0]
	s_nop 0
	v_pk_fma_f32 v[152:153], v[118:119], v[230:231], v[152:153] op_sel_hi:[1,0,1]
	v_mov_b32_e32 v154, v231
	v_pk_fma_f32 v[156:157], v[122:123], v[154:155], v[152:153] op_sel_hi:[1,0,1]
	ds_read_b128 v[224:227], v182 offset:5120
	s_waitcnt lgkmcnt(3)
	v_pk_fma_f32 v[156:157], v[108:109], v[232:233], v[156:157] op_sel_hi:[1,0,1]
	s_nop 0
	v_pk_fma_f32 v[152:153], v[110:111], v[232:233], v[156:157] op_sel:[0,1,0]
	s_nop 0
	v_pk_fma_f32 v[152:153], v[116:117], v[234:235], v[152:153] op_sel_hi:[1,0,1]
	v_mov_b32_e32 v154, v235
	v_pk_fma_f32 v[156:157], v[120:121], v[154:155], v[152:153] op_sel_hi:[1,0,1]
	ds_read_b128 v[228:231], v182 offset:6144
	s_waitcnt lgkmcnt(3)
	v_pk_fma_f32 v[156:157], v[96:97], v[236:237], v[156:157] op_sel_hi:[1,0,1]
	s_nop 0
	v_pk_fma_f32 v[152:153], v[98:99], v[236:237], v[156:157] op_sel:[0,1,0]
	s_nop 0
	v_pk_fma_f32 v[152:153], v[102:103], v[238:239], v[152:153] op_sel_hi:[1,0,1]
	v_mov_b32_e32 v154, v239
	v_pk_fma_f32 v[156:157], v[106:107], v[154:155], v[152:153] op_sel_hi:[1,0,1]
	ds_read_b128 v[232:235], v182 offset:7168
	s_waitcnt lgkmcnt(3)
	v_pk_fma_f32 v[156:157], v[92:93], v[240:241], v[156:157] op_sel_hi:[1,0,1]
	s_nop 0
	v_pk_fma_f32 v[152:153], v[94:95], v[240:241], v[156:157] op_sel:[0,1,0]
	s_nop 0
	v_pk_fma_f32 v[152:153], v[100:101], v[242:243], v[152:153] op_sel_hi:[1,0,1]
	v_mov_b32_e32 v154, v243
	v_pk_fma_f32 v[156:157], v[104:105], v[154:155], v[152:153] op_sel_hi:[1,0,1]
	ds_read_b128 v[236:239], v182 offset:8192
	s_waitcnt lgkmcnt(3)
	v_pk_fma_f32 v[156:157], v[80:81], v[224:225], v[156:157] op_sel_hi:[1,0,1]
	s_nop 0
	v_pk_fma_f32 v[152:153], v[82:83], v[224:225], v[156:157] op_sel:[0,1,0]
	s_nop 0
	v_pk_fma_f32 v[152:153], v[86:87], v[226:227], v[152:153] op_sel_hi:[1,0,1]
	v_mov_b32_e32 v154, v227
	v_pk_fma_f32 v[156:157], v[90:91], v[154:155], v[152:153] op_sel_hi:[1,0,1]
	ds_read_b128 v[240:243], v182 offset:9216
	s_waitcnt lgkmcnt(3)
	v_pk_fma_f32 v[156:157], v[76:77], v[228:229], v[156:157] op_sel_hi:[1,0,1]
	s_nop 0
	v_pk_fma_f32 v[152:153], v[78:79], v[228:229], v[156:157] op_sel:[0,1,0]
	s_nop 0
	v_pk_fma_f32 v[152:153], v[84:85], v[230:231], v[152:153] op_sel_hi:[1,0,1]
	v_mov_b32_e32 v154, v231
	v_pk_fma_f32 v[156:157], v[88:89], v[154:155], v[152:153] op_sel_hi:[1,0,1]
	ds_read_b128 v[224:227], v182 offset:10240
	s_waitcnt lgkmcnt(3)
	v_pk_fma_f32 v[156:157], v[68:69], v[232:233], v[156:157] op_sel_hi:[1,0,1]
	s_nop 0
	v_pk_fma_f32 v[152:153], v[70:71], v[232:233], v[156:157] op_sel:[0,1,0]
	s_nop 0
	v_pk_fma_f32 v[152:153], v[72:73], v[234:235], v[152:153] op_sel_hi:[1,0,1]
	v_mov_b32_e32 v154, v235
	v_pk_fma_f32 v[152:153], v[74:75], v[154:155], v[152:153] op_sel_hi:[1,0,1]
	ds_read_b128 v[228:231], v182 offset:11264
	s_waitcnt lgkmcnt(3)
	v_pk_fma_f32 v[158:159], v[124:125], v[236:237], 0 op_sel_hi:[1,0,0]
	s_nop 0
	v_pk_fma_f32 v[154:155], v[126:127], v[236:237], v[158:159] op_sel:[0,1,0]
	s_nop 0
	v_pk_fma_f32 v[154:155], v[128:129], v[238:239], v[154:155] op_sel_hi:[1,0,1]
	v_mov_b32_e32 v156, v239
	v_pk_fma_f32 v[158:159], v[130:131], v[156:157], v[154:155] op_sel_hi:[1,0,1]
	ds_read_b128 v[232:235], v182 offset:12288
	s_waitcnt lgkmcnt(3)
	v_pk_fma_f32 v[158:159], v[112:113], v[240:241], v[158:159] op_sel_hi:[1,0,1]
	s_nop 0
	v_pk_fma_f32 v[154:155], v[114:115], v[240:241], v[158:159] op_sel:[0,1,0]
	s_nop 0
	v_pk_fma_f32 v[154:155], v[118:119], v[242:243], v[154:155] op_sel_hi:[1,0,1]
	v_mov_b32_e32 v156, v243
	v_pk_fma_f32 v[158:159], v[122:123], v[156:157], v[154:155] op_sel_hi:[1,0,1]
	ds_read_b128 v[236:239], v182 offset:13312
	s_waitcnt lgkmcnt(3)
	v_pk_fma_f32 v[158:159], v[108:109], v[224:225], v[158:159] op_sel_hi:[1,0,1]
	s_nop 0
	v_pk_fma_f32 v[154:155], v[110:111], v[224:225], v[158:159] op_sel:[0,1,0]
	s_nop 0
	v_pk_fma_f32 v[154:155], v[116:117], v[226:227], v[154:155] op_sel_hi:[1,0,1]
	v_mov_b32_e32 v156, v227
	v_pk_fma_f32 v[158:159], v[120:121], v[156:157], v[154:155] op_sel_hi:[1,0,1]
	ds_read_b128 v[240:243], v182 offset:14336
	s_waitcnt lgkmcnt(3)
	v_pk_fma_f32 v[158:159], v[96:97], v[228:229], v[158:159] op_sel_hi:[1,0,1]
	s_nop 0
	v_pk_fma_f32 v[154:155], v[98:99], v[228:229], v[158:159] op_sel:[0,1,0]
	s_nop 0
	v_pk_fma_f32 v[154:155], v[102:103], v[230:231], v[154:155] op_sel_hi:[1,0,1]
	v_mov_b32_e32 v156, v231
	v_pk_fma_f32 v[158:159], v[106:107], v[156:157], v[154:155] op_sel_hi:[1,0,1]
	ds_read_b128 v[224:227], v182 offset:15360
	s_waitcnt lgkmcnt(3)
	v_pk_fma_f32 v[158:159], v[92:93], v[232:233], v[158:159] op_sel_hi:[1,0,1]
	s_nop 0
	v_pk_fma_f32 v[154:155], v[94:95], v[232:233], v[158:159] op_sel:[0,1,0]
	s_nop 0
	v_pk_fma_f32 v[154:155], v[100:101], v[234:235], v[154:155] op_sel_hi:[1,0,1]
	v_mov_b32_e32 v156, v235
	v_pk_fma_f32 v[158:159], v[104:105], v[156:157], v[154:155] op_sel_hi:[1,0,1]
	ds_read_b128 v[228:231], v182 offset:16384
	s_waitcnt lgkmcnt(3)
; #define LAS __attribute__((address_space(3)))
; __device__ __forceinline__ void phase_norm2(const Params& p, const Ctx& F, const int l) {
;     ...
; #pragma unroll
;         for (int e = 0; e < 16; ++e) { f32x2 a = {0.f, 0.f};
; #pragma unroll
;             for (int j = 0; j < 8; ++j) { const f32x4 w = *((const LAS f32x4*)(wr2 + e * DM) + F.lane + 64 * j);
; #pragma unroll
;                 for (int c = 0; c < 4; ++c) a += vv[j][c] * w[c]; }
;             lg[e] = a; }
	v_pk_fma_f32 v[158:159], v[80:81], v[236:237], v[158:159] op_sel_hi:[1,0,1]
	s_nop 0
	v_pk_fma_f32 v[154:155], v[82:83], v[236:237], v[158:159] op_sel:[0,1,0]
	s_nop 0
	v_pk_fma_f32 v[154:155], v[86:87], v[238:239], v[154:155] op_sel_hi:[1,0,1]
	v_mov_b32_e32 v156, v239
	v_pk_fma_f32 v[158:159], v[90:91], v[156:157], v[154:155] op_sel_hi:[1,0,1]
	ds_read_b128 v[232:235], v182 offset:17408
	s_waitcnt lgkmcnt(3)
	v_pk_fma_f32 v[158:159], v[76:77], v[240:241], v[158:159] op_sel_hi:[1,0,1]
	s_nop 0
	v_pk_fma_f32 v[154:155], v[78:79], v[240:241], v[158:159] op_sel:[0,1,0]
	s_nop 0
	v_pk_fma_f32 v[154:155], v[84:85], v[242:243], v[154:155] op_sel_hi:[1,0,1]
	v_mov_b32_e32 v156, v243
	v_pk_fma_f32 v[158:159], v[88:89], v[156:157], v[154:155] op_sel_hi:[1,0,1]
	ds_read_b128 v[236:239], v182 offset:18432
	s_waitcnt lgkmcnt(3)
	v_pk_fma_f32 v[158:159], v[68:69], v[224:225], v[158:159] op_sel_hi:[1,0,1]
	s_nop 0
	v_pk_fma_f32 v[154:155], v[70:71], v[224:225], v[158:159] op_sel:[0,1,0]
	s_nop 0
	v_pk_fma_f32 v[154:155], v[72:73], v[226:227], v[154:155] op_sel_hi:[1,0,1]
	v_mov_b32_e32 v156, v227
	v_pk_fma_f32 v[154:155], v[74:75], v[156:157], v[154:155] op_sel_hi:[1,0,1]
	ds_read_b128 v[240:243], v182 offset:19456
	s_waitcnt lgkmcnt(3)
	v_pk_fma_f32 v[160:161], v[124:125], v[228:229], 0 op_sel_hi:[1,0,0]
	s_nop 0
	v_pk_fma_f32 v[156:157], v[126:127], v[228:229], v[160:161] op_sel:[0,1,0]
	s_nop 0
	v_pk_fma_f32 v[156:157], v[128:129], v[230:231], v[156:157] op_sel_hi:[1,0,1]
	v_mov_b32_e32 v158, v231
	v_pk_fma_f32 v[160:161], v[130:131], v[158:159], v[156:157] op_sel_hi:[1,0,1]
	ds_read_b128 v[224:227], v182 offset:20480
	s_waitcnt lgkmcnt(3)
	v_pk_fma_f32 v[160:161], v[112:113], v[232:233], v[160:161] op_sel_hi:[1,0,1]
	s_nop 0
	v_pk_fma_f32 v[156:157], v[114:115], v[232:233], v[160:161] op_sel:[0,1,0]
	s_nop 0
	v_pk_fma_f32 v[156:157], v[118:119], v[234:235], v[156:157] op_sel_hi:[1,0,1]
	v_mov_b32_e32 v158, v235
	v_pk_fma_f32 v[160:161], v[122:123], v[158:159], v[156:157] op_sel_hi:[1,0,1]
	ds_read_b128 v[228:231], v182 offset:21504
	s_waitcnt lgkmcnt(3)
	v_pk_fma_f32 v[160:161], v[108:109], v[236:237], v[160:161] op_sel_hi:[1,0,1]
	s_nop 0
	v_pk_fma_f32 v[156:157], v[110:111], v[236:237], v[160:161] op_sel:[0,1,0]
	s_nop 0
	v_pk_fma_f32 v[156:157], v[116:117], v[238:239], v[156:157] op_sel_hi:[1,0,1]
	v_mov_b32_e32 v158, v239
	v_pk_fma_f32 v[160:161], v[120:121], v[158:159], v[156:157] op_sel_hi:[1,0,1]
	ds_read_b128 v[232:235], v182 offset:22528
	s_waitcnt lgkmcnt(3)
	v_pk_fma_f32 v[160:161], v[96:97], v[240:241], v[160:161] op_sel_hi:[1,0,1]
	s_nop 0
	v_pk_fma_f32 v[156:157], v[98:99], v[240:241], v[160:161] op_sel:[0,1,0]
	s_nop 0
	v_pk_fma_f32 v[156:157], v[102:103], v[242:243], v[156:157] op_sel_hi:[1,0,1]
	v_mov_b32_e32 v158, v243
	v_pk_fma_f32 v[160:161], v[106:107], v[158:159], v[156:157] op_sel_hi:[1,0,1]
	ds_read_b128 v[236:239], v182 offset:23552
	s_waitcnt lgkmcnt(3)
	v_pk_fma_f32 v[160:161], v[92:93], v[224:225], v[160:161] op_sel_hi:[1,0,1]
	s_nop 0
	v_pk_fma_f32 v[156:157], v[94:95], v[224:225], v[160:161] op_sel:[0,1,0]
	s_nop 0
	v_pk_fma_f32 v[156:157], v[100:101], v[226:227], v[156:157] op_sel_hi:[1,0,1]
	v_mov_b32_e32 v158, v227
	v_pk_fma_f32 v[160:161], v[104:105], v[158:159], v[156:157] op_sel_hi:[1,0,1]
	ds_read_b128 v[240:243], v182 offset:24576
	s_waitcnt lgkmcnt(3)
	v_pk_fma_f32 v[160:161], v[80:81], v[228:229], v[160:161] op_sel_hi:[1,0,1]
	s_nop 0
	v_pk_fma_f32 v[156:157], v[82:83], v[228:229], v[160:161] op_sel:[0,1,0]
	s_nop 0
	v_pk_fma_f32 v[156:157], v[86:87], v[230:231], v[156:157] op_sel_hi:[1,0,1]
	v_mov_b32_e32 v158, v231
	v_pk_fma_f32 v[160:161], v[90:91], v[158:159], v[156:157] op_sel_hi:[1,0,1]
	ds_read_b128 v[224:227], v182 offset:25600
	s_waitcnt lgkmcnt(3)
	v_pk_fma_f32 v[160:161], v[76:77], v[232:233], v[160:161] op_sel_hi:[1,0,1]
	s_nop 0
	v_pk_fma_f32 v[156:157], v[78:79], v[232:233], v[160:161] op_sel:[0,1,0]
	s_nop 0
	v_pk_fma_f32 v[156:157], v[84:85], v[234:235], v[156:157] op_sel_hi:[1,0,1]
	v_mov_b32_e32 v158, v235
	v_pk_fma_f32 v[160:161], v[88:89], v[158:159], v[156:157] op_sel_hi:[1,0,1]
	ds_read_b128 v[228:231], v182 offset:26624
	s_waitcnt lgkmcnt(3)
	v_pk_fma_f32 v[160:161], v[68:69], v[236:237], v[160:161] op_sel_hi:[1,0,1]
	s_nop 0
	v_pk_fma_f32 v[156:157], v[70:71], v[236:237], v[160:161] op_sel:[0,1,0]
	s_nop 0
	v_pk_fma_f32 v[156:157], v[72:73], v[238:239], v[156:157] op_sel_hi:[1,0,1]
	v_mov_b32_e32 v158, v239
	v_pk_fma_f32 v[156:157], v[74:75], v[158:159], v[156:157] op_sel_hi:[1,0,1]
	ds_read_b128 v[232:235], v182 offset:27648
	s_waitcnt lgkmcnt(3)
	v_pk_fma_f32 v[162:163], v[124:125], v[240:241], 0 op_sel_hi:[1,0,0]
	s_nop 0
	v_pk_fma_f32 v[158:159], v[126:127], v[240:241], v[162:163] op_sel:[0,1,0]
	s_nop 0
	v_pk_fma_f32 v[158:159], v[128:129], v[242:243], v[158:159] op_sel_hi:[1,0,1]
	v_mov_b32_e32 v160, v243
	v_pk_fma_f32 v[162:163], v[130:131], v[160:161], v[158:159] op_sel_hi:[1,0,1]
	ds_read_b128 v[236:239], v182 offset:28672
	s_waitcnt lgkmcnt(3)
	v_pk_fma_f32 v[162:163], v[112:113], v[224:225], v[162:163] op_sel_hi:[1,0,1]
	s_nop 0
	v_pk_fma_f32 v[158:159], v[114:115], v[224:225], v[162:163] op_sel:[0,1,0]
	s_nop 0
	v_pk_fma_f32 v[158:159], v[118:119], v[226:227], v[158:159] op_sel_hi:[1,0,1]
	v_mov_b32_e32 v160, v227
	v_pk_fma_f32 v[162:163], v[122:123], v[160:161], v[158:159] op_sel_hi:[1,0,1]
	ds_read_b128 v[240:243], v182 offset:29696
	s_waitcnt lgkmcnt(3)
	v_pk_fma_f32 v[162:163], v[108:109], v[228:229], v[162:163] op_sel_hi:[1,0,1]
	s_nop 0
	v_pk_fma_f32 v[158:159], v[110:111], v[228:229], v[162:163] op_sel:[0,1,0]
	s_nop 0
	v_pk_fma_f32 v[158:159], v[116:117], v[230:231], v[158:159] op_sel_hi:[1,0,1]
	v_mov_b32_e32 v160, v231
	v_pk_fma_f32 v[162:163], v[120:121], v[160:161], v[158:159] op_sel_hi:[1,0,1]
	ds_read_b128 v[224:227], v182 offset:30720
	s_waitcnt lgkmcnt(3)
; #define LAS __attribute__((address_space(3)))
; __device__ __forceinline__ void phase_norm2(const Params& p, const Ctx& F, const int l) {
;     ...
; #pragma unroll
;         for (int e = 0; e < 16; ++e) { f32x2 a = {0.f, 0.f};
; #pragma unroll
;             for (int j = 0; j < 8; ++j) { const f32x4 w = *((const LAS f32x4*)(wr2 + e * DM) + F.lane + 64 * j);
; #pragma unroll
;                 for (int c = 0; c < 4; ++c) a += vv[j][c] * w[c]; }
;             lg[e] = a; }
	v_pk_fma_f32 v[162:163], v[96:97], v[232:233], v[162:163] op_sel_hi:[1,0,1]
	s_nop 0
	v_pk_fma_f32 v[158:159], v[98:99], v[232:233], v[162:163] op_sel:[0,1,0]
	s_nop 0
	v_pk_fma_f32 v[158:159], v[102:103], v[234:235], v[158:159] op_sel_hi:[1,0,1]
	v_mov_b32_e32 v160, v235
	v_pk_fma_f32 v[162:163], v[106:107], v[160:161], v[158:159] op_sel_hi:[1,0,1]
	ds_read_b128 v[228:231], v182 offset:31744
	s_waitcnt lgkmcnt(3)
	v_pk_fma_f32 v[162:163], v[92:93], v[236:237], v[162:163] op_sel_hi:[1,0,1]
	s_nop 0
	v_pk_fma_f32 v[158:159], v[94:95], v[236:237], v[162:163] op_sel:[0,1,0]
	s_nop 0
	v_pk_fma_f32 v[158:159], v[100:101], v[238:239], v[158:159] op_sel_hi:[1,0,1]
	v_mov_b32_e32 v160, v239
	v_pk_fma_f32 v[162:163], v[104:105], v[160:161], v[158:159] op_sel_hi:[1,0,1]
	ds_read_b128 v[232:235], v182 offset:32768
	s_waitcnt lgkmcnt(3)
	v_pk_fma_f32 v[162:163], v[80:81], v[240:241], v[162:163] op_sel_hi:[1,0,1]
	s_nop 0
	v_pk_fma_f32 v[158:159], v[82:83], v[240:241], v[162:163] op_sel:[0,1,0]
	s_nop 0
	v_pk_fma_f32 v[158:159], v[86:87], v[242:243], v[158:159] op_sel_hi:[1,0,1]
	v_mov_b32_e32 v160, v243
	v_pk_fma_f32 v[162:163], v[90:91], v[160:161], v[158:159] op_sel_hi:[1,0,1]
	ds_read_b128 v[236:239], v182 offset:33792
	s_waitcnt lgkmcnt(3)
	v_pk_fma_f32 v[162:163], v[76:77], v[224:225], v[162:163] op_sel_hi:[1,0,1]
	s_nop 0
	v_pk_fma_f32 v[158:159], v[78:79], v[224:225], v[162:163] op_sel:[0,1,0]
	s_nop 0
	v_pk_fma_f32 v[158:159], v[84:85], v[226:227], v[158:159] op_sel_hi:[1,0,1]
	v_mov_b32_e32 v160, v227
	v_pk_fma_f32 v[162:163], v[88:89], v[160:161], v[158:159] op_sel_hi:[1,0,1]
	ds_read_b128 v[240:243], v182 offset:34816
	s_waitcnt lgkmcnt(3)
	v_pk_fma_f32 v[162:163], v[68:69], v[228:229], v[162:163] op_sel_hi:[1,0,1]
	s_nop 0
	v_pk_fma_f32 v[158:159], v[70:71], v[228:229], v[162:163] op_sel:[0,1,0]
	s_nop 0
	v_pk_fma_f32 v[158:159], v[72:73], v[230:231], v[158:159] op_sel_hi:[1,0,1]
	v_mov_b32_e32 v160, v231
	v_pk_fma_f32 v[158:159], v[74:75], v[160:161], v[158:159] op_sel_hi:[1,0,1]
	ds_read_b128 v[224:227], v182 offset:35840
	s_waitcnt lgkmcnt(3)
	v_pk_fma_f32 v[164:165], v[124:125], v[232:233], 0 op_sel_hi:[1,0,0]
	s_nop 0
	v_pk_fma_f32 v[160:161], v[126:127], v[232:233], v[164:165] op_sel:[0,1,0]
	s_nop 0
	v_pk_fma_f32 v[160:161], v[128:129], v[234:235], v[160:161] op_sel_hi:[1,0,1]
	v_mov_b32_e32 v162, v235
	v_pk_fma_f32 v[164:165], v[130:131], v[162:163], v[160:161] op_sel_hi:[1,0,1]
	ds_read_b128 v[228:231], v182 offset:36864
	s_waitcnt lgkmcnt(3)
	v_pk_fma_f32 v[164:165], v[112:113], v[236:237], v[164:165] op_sel_hi:[1,0,1]
	s_nop 0
	v_pk_fma_f32 v[160:161], v[114:115], v[236:237], v[164:165] op_sel:[0,1,0]
	s_nop 0
	v_pk_fma_f32 v[160:161], v[118:119], v[238:239], v[160:161] op_sel_hi:[1,0,1]
	v_mov_b32_e32 v162, v239
	v_pk_fma_f32 v[164:165], v[122:123], v[162:163], v[160:161] op_sel_hi:[1,0,1]
	ds_read_b128 v[232:235], v182 offset:37888
	s_waitcnt lgkmcnt(3)
	v_pk_fma_f32 v[164:165], v[108:109], v[240:241], v[164:165] op_sel_hi:[1,0,1]
	s_nop 0
	v_pk_fma_f32 v[160:161], v[110:111], v[240:241], v[164:165] op_sel:[0,1,0]
	s_nop 0
	v_pk_fma_f32 v[160:161], v[116:117], v[242:243], v[160:161] op_sel_hi:[1,0,1]
	v_mov_b32_e32 v162, v243
	v_pk_fma_f32 v[164:165], v[120:121], v[162:163], v[160:161] op_sel_hi:[1,0,1]
	ds_read_b128 v[236:239], v182 offset:38912
	s_waitcnt lgkmcnt(3)
	v_pk_fma_f32 v[164:165], v[96:97], v[224:225], v[164:165] op_sel_hi:[1,0,1]
	s_nop 0
	v_pk_fma_f32 v[160:161], v[98:99], v[224:225], v[164:165] op_sel:[0,1,0]
	s_nop 0
	v_pk_fma_f32 v[160:161], v[102:103], v[226:227], v[160:161] op_sel_hi:[1,0,1]
	v_mov_b32_e32 v162, v227
	v_pk_fma_f32 v[164:165], v[106:107], v[162:163], v[160:161] op_sel_hi:[1,0,1]
	ds_read_b128 v[240:243], v182 offset:39936
	s_waitcnt lgkmcnt(3)
	v_pk_fma_f32 v[164:165], v[92:93], v[228:229], v[164:165] op_sel_hi:[1,0,1]
	s_nop 0
	v_pk_fma_f32 v[160:161], v[94:95], v[228:229], v[164:165] op_sel:[0,1,0]
	s_nop 0
	v_pk_fma_f32 v[160:161], v[100:101], v[230:231], v[160:161] op_sel_hi:[1,0,1]
	v_mov_b32_e32 v162, v231
	v_pk_fma_f32 v[164:165], v[104:105], v[162:163], v[160:161] op_sel_hi:[1,0,1]
	ds_read_b128 v[224:227], v182 offset:40960
	s_waitcnt lgkmcnt(3)
	v_pk_fma_f32 v[164:165], v[80:81], v[232:233], v[164:165] op_sel_hi:[1,0,1]
	s_nop 0
	v_pk_fma_f32 v[160:161], v[82:83], v[232:233], v[164:165] op_sel:[0,1,0]
	s_nop 0
	v_pk_fma_f32 v[160:161], v[86:87], v[234:235], v[160:161] op_sel_hi:[1,0,1]
	v_mov_b32_e32 v162, v235
	v_pk_fma_f32 v[164:165], v[90:91], v[162:163], v[160:161] op_sel_hi:[1,0,1]
	ds_read_b128 v[228:231], v182 offset:41984
	s_waitcnt lgkmcnt(3)
	v_pk_fma_f32 v[164:165], v[76:77], v[236:237], v[164:165] op_sel_hi:[1,0,1]
	s_nop 0
	v_pk_fma_f32 v[160:161], v[78:79], v[236:237], v[164:165] op_sel:[0,1,0]
	s_nop 0
	v_pk_fma_f32 v[160:161], v[84:85], v[238:239], v[160:161] op_sel_hi:[1,0,1]
	v_mov_b32_e32 v162, v239
	v_pk_fma_f32 v[164:165], v[88:89], v[162:163], v[160:161] op_sel_hi:[1,0,1]
	ds_read_b128 v[232:235], v182 offset:43008
	s_waitcnt lgkmcnt(3)
	v_pk_fma_f32 v[164:165], v[68:69], v[240:241], v[164:165] op_sel_hi:[1,0,1]
	s_nop 0
	v_pk_fma_f32 v[160:161], v[70:71], v[240:241], v[164:165] op_sel:[0,1,0]
	s_nop 0
	v_pk_fma_f32 v[160:161], v[72:73], v[242:243], v[160:161] op_sel_hi:[1,0,1]
	v_mov_b32_e32 v162, v243
	v_pk_fma_f32 v[160:161], v[74:75], v[162:163], v[160:161] op_sel_hi:[1,0,1]
	ds_read_b128 v[236:239], v182 offset:44032
	s_waitcnt lgkmcnt(3)
	v_pk_fma_f32 v[166:167], v[124:125], v[224:225], 0 op_sel_hi:[1,0,0]
	s_nop 0
	v_pk_fma_f32 v[162:163], v[126:127], v[224:225], v[166:167] op_sel:[0,1,0]
	s_nop 0
	v_pk_fma_f32 v[162:163], v[128:129], v[226:227], v[162:163] op_sel_hi:[1,0,1]
	v_mov_b32_e32 v164, v227
	v_pk_fma_f32 v[166:167], v[130:131], v[164:165], v[162:163] op_sel_hi:[1,0,1]
	ds_read_b128 v[240:243], v182 offset:45056
	s_waitcnt lgkmcnt(3)
; #define LAS __attribute__((address_space(3)))
; __device__ __forceinline__ void phase_norm2(const Params& p, const Ctx& F, const int l) {
;     ...
; #pragma unroll
;         for (int e = 0; e < 16; ++e) { f32x2 a = {0.f, 0.f};
; #pragma unroll
;             for (int j = 0; j < 8; ++j) { const f32x4 w = *((const LAS f32x4*)(wr2 + e * DM) + F.lane + 64 * j);
; #pragma unroll
;                 for (int c = 0; c < 4; ++c) a += vv[j][c] * w[c]; }
;             lg[e] = a; }
	v_pk_fma_f32 v[166:167], v[112:113], v[228:229], v[166:167] op_sel_hi:[1,0,1]
	s_nop 0
	v_pk_fma_f32 v[162:163], v[114:115], v[228:229], v[166:167] op_sel:[0,1,0]
	s_nop 0
	v_pk_fma_f32 v[162:163], v[118:119], v[230:231], v[162:163] op_sel_hi:[1,0,1]
	v_mov_b32_e32 v164, v231
	v_pk_fma_f32 v[166:167], v[122:123], v[164:165], v[162:163] op_sel_hi:[1,0,1]
	ds_read_b128 v[224:227], v182 offset:46080
	s_waitcnt lgkmcnt(3)
	v_pk_fma_f32 v[166:167], v[108:109], v[232:233], v[166:167] op_sel_hi:[1,0,1]
	s_nop 0
	v_pk_fma_f32 v[162:163], v[110:111], v[232:233], v[166:167] op_sel:[0,1,0]
	s_nop 0
	v_pk_fma_f32 v[162:163], v[116:117], v[234:235], v[162:163] op_sel_hi:[1,0,1]
	v_mov_b32_e32 v164, v235
	v_pk_fma_f32 v[166:167], v[120:121], v[164:165], v[162:163] op_sel_hi:[1,0,1]
	ds_read_b128 v[228:231], v182 offset:47104
	s_waitcnt lgkmcnt(3)
	v_pk_fma_f32 v[166:167], v[96:97], v[236:237], v[166:167] op_sel_hi:[1,0,1]
	s_nop 0
	v_pk_fma_f32 v[162:163], v[98:99], v[236:237], v[166:167] op_sel:[0,1,0]
	s_nop 0
	v_pk_fma_f32 v[162:163], v[102:103], v[238:239], v[162:163] op_sel_hi:[1,0,1]
	v_mov_b32_e32 v164, v239
	v_pk_fma_f32 v[166:167], v[106:107], v[164:165], v[162:163] op_sel_hi:[1,0,1]
	ds_read_b128 v[232:235], v182 offset:48128
	s_waitcnt lgkmcnt(3)
	v_pk_fma_f32 v[166:167], v[92:93], v[240:241], v[166:167] op_sel_hi:[1,0,1]
	s_nop 0
	v_pk_fma_f32 v[162:163], v[94:95], v[240:241], v[166:167] op_sel:[0,1,0]
	s_nop 0
	v_pk_fma_f32 v[162:163], v[100:101], v[242:243], v[162:163] op_sel_hi:[1,0,1]
	v_mov_b32_e32 v164, v243
	v_pk_fma_f32 v[166:167], v[104:105], v[164:165], v[162:163] op_sel_hi:[1,0,1]
	ds_read_b128 v[236:239], v182 offset:49152
	s_waitcnt lgkmcnt(3)
	v_pk_fma_f32 v[166:167], v[80:81], v[224:225], v[166:167] op_sel_hi:[1,0,1]
	s_nop 0
	v_pk_fma_f32 v[162:163], v[82:83], v[224:225], v[166:167] op_sel:[0,1,0]
	s_nop 0
	v_pk_fma_f32 v[162:163], v[86:87], v[226:227], v[162:163] op_sel_hi:[1,0,1]
	v_mov_b32_e32 v164, v227
	v_pk_fma_f32 v[166:167], v[90:91], v[164:165], v[162:163] op_sel_hi:[1,0,1]
	ds_read_b128 v[240:243], v182 offset:50176
	s_waitcnt lgkmcnt(3)
	v_pk_fma_f32 v[166:167], v[76:77], v[228:229], v[166:167] op_sel_hi:[1,0,1]
	s_nop 0
	v_pk_fma_f32 v[162:163], v[78:79], v[228:229], v[166:167] op_sel:[0,1,0]
	s_nop 0
	v_pk_fma_f32 v[162:163], v[84:85], v[230:231], v[162:163] op_sel_hi:[1,0,1]
	v_mov_b32_e32 v164, v231
	v_pk_fma_f32 v[166:167], v[88:89], v[164:165], v[162:163] op_sel_hi:[1,0,1]
	ds_read_b128 v[224:227], v182 offset:51200
	s_waitcnt lgkmcnt(3)
	v_pk_fma_f32 v[166:167], v[68:69], v[232:233], v[166:167] op_sel_hi:[1,0,1]
	s_nop 0
	v_pk_fma_f32 v[162:163], v[70:71], v[232:233], v[166:167] op_sel:[0,1,0]
	s_nop 0
	v_pk_fma_f32 v[162:163], v[72:73], v[234:235], v[162:163] op_sel_hi:[1,0,1]
	v_mov_b32_e32 v164, v235
	v_pk_fma_f32 v[162:163], v[74:75], v[164:165], v[162:163] op_sel_hi:[1,0,1]
	ds_read_b128 v[228:231], v182 offset:52224
	s_waitcnt lgkmcnt(3)
	v_pk_fma_f32 v[168:169], v[124:125], v[236:237], 0 op_sel_hi:[1,0,0]
	s_nop 0
	v_pk_fma_f32 v[164:165], v[126:127], v[236:237], v[168:169] op_sel:[0,1,0]
	s_nop 0
	v_pk_fma_f32 v[164:165], v[128:129], v[238:239], v[164:165] op_sel_hi:[1,0,1]
	v_mov_b32_e32 v166, v239
	v_pk_fma_f32 v[168:169], v[130:131], v[166:167], v[164:165] op_sel_hi:[1,0,1]
	ds_read_b128 v[232:235], v182 offset:53248
	s_waitcnt lgkmcnt(3)
	v_pk_fma_f32 v[168:169], v[112:113], v[240:241], v[168:169] op_sel_hi:[1,0,1]
	s_nop 0
	v_pk_fma_f32 v[164:165], v[114:115], v[240:241], v[168:169] op_sel:[0,1,0]
	s_nop 0
	v_pk_fma_f32 v[164:165], v[118:119], v[242:243], v[164:165] op_sel_hi:[1,0,1]
	v_mov_b32_e32 v166, v243
	v_pk_fma_f32 v[168:169], v[122:123], v[166:167], v[164:165] op_sel_hi:[1,0,1]
	ds_read_b128 v[236:239], v182 offset:54272
	s_waitcnt lgkmcnt(3)
	v_pk_fma_f32 v[168:169], v[108:109], v[224:225], v[168:169] op_sel_hi:[1,0,1]
	s_nop 0
	v_pk_fma_f32 v[164:165], v[110:111], v[224:225], v[168:169] op_sel:[0,1,0]
	s_nop 0
	v_pk_fma_f32 v[164:165], v[116:117], v[226:227], v[164:165] op_sel_hi:[1,0,1]
	v_mov_b32_e32 v166, v227
	v_pk_fma_f32 v[168:169], v[120:121], v[166:167], v[164:165] op_sel_hi:[1,0,1]
	ds_read_b128 v[240:243], v182 offset:55296
	s_waitcnt lgkmcnt(3)
	v_pk_fma_f32 v[168:169], v[96:97], v[228:229], v[168:169] op_sel_hi:[1,0,1]
	s_nop 0
	v_pk_fma_f32 v[164:165], v[98:99], v[228:229], v[168:169] op_sel:[0,1,0]
	s_nop 0
	v_pk_fma_f32 v[164:165], v[102:103], v[230:231], v[164:165] op_sel_hi:[1,0,1]
	v_mov_b32_e32 v166, v231
	v_pk_fma_f32 v[168:169], v[106:107], v[166:167], v[164:165] op_sel_hi:[1,0,1]
	ds_read_b128 v[224:227], v182 offset:56320
	s_waitcnt lgkmcnt(3)
	v_pk_fma_f32 v[168:169], v[92:93], v[232:233], v[168:169] op_sel_hi:[1,0,1]
	s_nop 0
	v_pk_fma_f32 v[164:165], v[94:95], v[232:233], v[168:169] op_sel:[0,1,0]
	s_nop 0
	v_pk_fma_f32 v[164:165], v[100:101], v[234:235], v[164:165] op_sel_hi:[1,0,1]
	v_mov_b32_e32 v166, v235
	v_pk_fma_f32 v[168:169], v[104:105], v[166:167], v[164:165] op_sel_hi:[1,0,1]
	ds_read_b128 v[228:231], v182 offset:57344
	s_waitcnt lgkmcnt(3)
	v_pk_fma_f32 v[168:169], v[80:81], v[236:237], v[168:169] op_sel_hi:[1,0,1]
	s_nop 0
	v_pk_fma_f32 v[164:165], v[82:83], v[236:237], v[168:169] op_sel:[0,1,0]
	s_nop 0
	v_pk_fma_f32 v[164:165], v[86:87], v[238:239], v[164:165] op_sel_hi:[1,0,1]
	v_mov_b32_e32 v166, v239
	v_pk_fma_f32 v[168:169], v[90:91], v[166:167], v[164:165] op_sel_hi:[1,0,1]
	ds_read_b128 v[232:235], v182 offset:58368
	s_waitcnt lgkmcnt(3)
; #define LAS __attribute__((address_space(3)))
; __device__ __forceinline__ void phase_norm2(const Params& p, const Ctx& F, const int l) {
;     ...
; #pragma unroll
;         for (int e = 0; e < 16; ++e) { f32x2 a = {0.f, 0.f};
; #pragma unroll
;             for (int j = 0; j < 8; ++j) { const f32x4 w = *((const LAS f32x4*)(wr2 + e * DM) + F.lane + 64 * j);
; #pragma unroll
;                 for (int c = 0; c < 4; ++c) a += vv[j][c] * w[c]; }
;             lg[e] = a; }
	v_pk_fma_f32 v[168:169], v[76:77], v[240:241], v[168:169] op_sel_hi:[1,0,1]
	s_nop 0
	v_pk_fma_f32 v[164:165], v[78:79], v[240:241], v[168:169] op_sel:[0,1,0]
	s_nop 0
	v_pk_fma_f32 v[164:165], v[84:85], v[242:243], v[164:165] op_sel_hi:[1,0,1]
	v_mov_b32_e32 v166, v243
	v_pk_fma_f32 v[168:169], v[88:89], v[166:167], v[164:165] op_sel_hi:[1,0,1]
	ds_read_b128 v[236:239], v182 offset:59392
	s_waitcnt lgkmcnt(3)
	v_pk_fma_f32 v[168:169], v[68:69], v[224:225], v[168:169] op_sel_hi:[1,0,1]
	s_nop 0
	v_pk_fma_f32 v[164:165], v[70:71], v[224:225], v[168:169] op_sel:[0,1,0]
	s_nop 0
	v_pk_fma_f32 v[164:165], v[72:73], v[226:227], v[164:165] op_sel_hi:[1,0,1]
	v_mov_b32_e32 v166, v227
	v_pk_fma_f32 v[164:165], v[74:75], v[166:167], v[164:165] op_sel_hi:[1,0,1]
	ds_read_b128 v[240:243], v182 offset:60416
	s_waitcnt lgkmcnt(3)
	v_pk_fma_f32 v[170:171], v[124:125], v[228:229], 0 op_sel_hi:[1,0,0]
	s_nop 0
	v_pk_fma_f32 v[166:167], v[126:127], v[228:229], v[170:171] op_sel:[0,1,0]
	s_nop 0
	v_pk_fma_f32 v[166:167], v[128:129], v[230:231], v[166:167] op_sel_hi:[1,0,1]
	v_mov_b32_e32 v168, v231
	v_pk_fma_f32 v[170:171], v[130:131], v[168:169], v[166:167] op_sel_hi:[1,0,1]
	ds_read_b128 v[224:227], v182 offset:61440
	s_waitcnt lgkmcnt(3)
	v_pk_fma_f32 v[170:171], v[112:113], v[232:233], v[170:171] op_sel_hi:[1,0,1]
	s_nop 0
	v_pk_fma_f32 v[166:167], v[114:115], v[232:233], v[170:171] op_sel:[0,1,0]
	s_nop 0
	v_pk_fma_f32 v[166:167], v[118:119], v[234:235], v[166:167] op_sel_hi:[1,0,1]
	v_mov_b32_e32 v168, v235
	v_pk_fma_f32 v[170:171], v[122:123], v[168:169], v[166:167] op_sel_hi:[1,0,1]
	ds_read_b128 v[228:231], v182 offset:62464
	s_waitcnt lgkmcnt(3)
	v_pk_fma_f32 v[170:171], v[108:109], v[236:237], v[170:171] op_sel_hi:[1,0,1]
	s_nop 0
	v_pk_fma_f32 v[166:167], v[110:111], v[236:237], v[170:171] op_sel:[0,1,0]
	s_nop 0
	v_pk_fma_f32 v[166:167], v[116:117], v[238:239], v[166:167] op_sel_hi:[1,0,1]
	v_mov_b32_e32 v168, v239
	v_pk_fma_f32 v[170:171], v[120:121], v[168:169], v[166:167] op_sel_hi:[1,0,1]
	ds_read_b128 v[232:235], v182 offset:63488
	s_waitcnt lgkmcnt(3)
	v_pk_fma_f32 v[170:171], v[96:97], v[240:241], v[170:171] op_sel_hi:[1,0,1]
	s_nop 0
	v_pk_fma_f32 v[166:167], v[98:99], v[240:241], v[170:171] op_sel:[0,1,0]
	s_nop 0
	v_pk_fma_f32 v[166:167], v[102:103], v[242:243], v[166:167] op_sel_hi:[1,0,1]
	v_mov_b32_e32 v168, v243
	v_pk_fma_f32 v[170:171], v[106:107], v[168:169], v[166:167] op_sel_hi:[1,0,1]
	ds_read_b128 v[236:239], v182 offset:64512
	s_waitcnt lgkmcnt(3)
	v_pk_fma_f32 v[170:171], v[92:93], v[224:225], v[170:171] op_sel_hi:[1,0,1]
	s_nop 0
	v_pk_fma_f32 v[166:167], v[94:95], v[224:225], v[170:171] op_sel:[0,1,0]
	s_nop 0
	v_pk_fma_f32 v[166:167], v[100:101], v[226:227], v[166:167] op_sel_hi:[1,0,1]
	v_mov_b32_e32 v168, v227
	v_pk_fma_f32 v[170:171], v[104:105], v[168:169], v[166:167] op_sel_hi:[1,0,1]
	ds_read_b128 v[240:243], v244
	s_waitcnt lgkmcnt(3)
	v_pk_fma_f32 v[170:171], v[80:81], v[228:229], v[170:171] op_sel_hi:[1,0,1]
	s_nop 0
	v_pk_fma_f32 v[166:167], v[82:83], v[228:229], v[170:171] op_sel:[0,1,0]
	s_nop 0
	v_pk_fma_f32 v[166:167], v[86:87], v[230:231], v[166:167] op_sel_hi:[1,0,1]
	v_mov_b32_e32 v168, v231
	v_pk_fma_f32 v[170:171], v[90:91], v[168:169], v[166:167] op_sel_hi:[1,0,1]
	ds_read_b128 v[224:227], v244 offset:1024
	s_waitcnt lgkmcnt(3)
	v_pk_fma_f32 v[170:171], v[76:77], v[232:233], v[170:171] op_sel_hi:[1,0,1]
	s_nop 0
	v_pk_fma_f32 v[166:167], v[78:79], v[232:233], v[170:171] op_sel:[0,1,0]
	s_nop 0
	v_pk_fma_f32 v[166:167], v[84:85], v[234:235], v[166:167] op_sel_hi:[1,0,1]
	v_mov_b32_e32 v168, v235
	v_pk_fma_f32 v[170:171], v[88:89], v[168:169], v[166:167] op_sel_hi:[1,0,1]
	ds_read_b128 v[228:231], v244 offset:2048
	s_waitcnt lgkmcnt(3)
	v_pk_fma_f32 v[170:171], v[68:69], v[236:237], v[170:171] op_sel_hi:[1,0,1]
	s_nop 0
	v_pk_fma_f32 v[166:167], v[70:71], v[236:237], v[170:171] op_sel:[0,1,0]
	s_nop 0
	v_pk_fma_f32 v[166:167], v[72:73], v[238:239], v[166:167] op_sel_hi:[1,0,1]
	v_mov_b32_e32 v168, v239
	v_pk_fma_f32 v[166:167], v[74:75], v[168:169], v[166:167] op_sel_hi:[1,0,1]
	ds_read_b128 v[232:235], v244 offset:3072
	s_waitcnt lgkmcnt(3)
	v_pk_fma_f32 v[172:173], v[124:125], v[240:241], 0 op_sel_hi:[1,0,0]
	s_nop 0
	v_pk_fma_f32 v[168:169], v[126:127], v[240:241], v[172:173] op_sel:[0,1,0]
	s_nop 0
	v_pk_fma_f32 v[168:169], v[128:129], v[242:243], v[168:169] op_sel_hi:[1,0,1]
	v_mov_b32_e32 v170, v243
	v_pk_fma_f32 v[172:173], v[130:131], v[170:171], v[168:169] op_sel_hi:[1,0,1]
	ds_read_b128 v[236:239], v244 offset:4096
	s_waitcnt lgkmcnt(3)
	v_pk_fma_f32 v[172:173], v[112:113], v[224:225], v[172:173] op_sel_hi:[1,0,1]
	s_nop 0
	v_pk_fma_f32 v[168:169], v[114:115], v[224:225], v[172:173] op_sel:[0,1,0]
	s_nop 0
	v_pk_fma_f32 v[168:169], v[118:119], v[226:227], v[168:169] op_sel_hi:[1,0,1]
	v_mov_b32_e32 v170, v227
	v_pk_fma_f32 v[172:173], v[122:123], v[170:171], v[168:169] op_sel_hi:[1,0,1]
	ds_read_b128 v[240:243], v244 offset:5120
	s_waitcnt lgkmcnt(3)
	v_pk_fma_f32 v[172:173], v[108:109], v[228:229], v[172:173] op_sel_hi:[1,0,1]
	s_nop 0
	v_pk_fma_f32 v[168:169], v[110:111], v[228:229], v[172:173] op_sel:[0,1,0]
	s_nop 0
	v_pk_fma_f32 v[168:169], v[116:117], v[230:231], v[168:169] op_sel_hi:[1,0,1]
	v_mov_b32_e32 v170, v231
	v_pk_fma_f32 v[172:173], v[120:121], v[170:171], v[168:169] op_sel_hi:[1,0,1]
	ds_read_b128 v[224:227], v244 offset:6144
	s_waitcnt lgkmcnt(3)
	v_pk_fma_f32 v[172:173], v[96:97], v[232:233], v[172:173] op_sel_hi:[1,0,1]
	s_nop 0
	v_pk_fma_f32 v[168:169], v[98:99], v[232:233], v[172:173] op_sel:[0,1,0]
	s_nop 0
	v_pk_fma_f32 v[168:169], v[102:103], v[234:235], v[168:169] op_sel_hi:[1,0,1]
	v_mov_b32_e32 v170, v235
	v_pk_fma_f32 v[172:173], v[106:107], v[170:171], v[168:169] op_sel_hi:[1,0,1]
	ds_read_b128 v[228:231], v244 offset:7168
	s_waitcnt lgkmcnt(3)
; #define LAS __attribute__((address_space(3)))
; __device__ __forceinline__ void phase_norm2(const Params& p, const Ctx& F, const int l) {
;     ...
; #pragma unroll
;         for (int e = 0; e < 16; ++e) { f32x2 a = {0.f, 0.f};
; #pragma unroll
;             for (int j = 0; j < 8; ++j) { const f32x4 w = *((const LAS f32x4*)(wr2 + e * DM) + F.lane + 64 * j);
; #pragma unroll
;                 for (int c = 0; c < 4; ++c) a += vv[j][c] * w[c]; }
;             lg[e] = a; }
	v_pk_fma_f32 v[172:173], v[92:93], v[236:237], v[172:173] op_sel_hi:[1,0,1]
	s_nop 0
	v_pk_fma_f32 v[168:169], v[94:95], v[236:237], v[172:173] op_sel:[0,1,0]
	s_nop 0
	v_pk_fma_f32 v[168:169], v[100:101], v[238:239], v[168:169] op_sel_hi:[1,0,1]
	v_mov_b32_e32 v170, v239
	v_pk_fma_f32 v[172:173], v[104:105], v[170:171], v[168:169] op_sel_hi:[1,0,1]
	ds_read_b128 v[232:235], v244 offset:8192
	s_waitcnt lgkmcnt(3)
	v_pk_fma_f32 v[172:173], v[80:81], v[240:241], v[172:173] op_sel_hi:[1,0,1]
	s_nop 0
	v_pk_fma_f32 v[168:169], v[82:83], v[240:241], v[172:173] op_sel:[0,1,0]
	s_nop 0
	v_pk_fma_f32 v[168:169], v[86:87], v[242:243], v[168:169] op_sel_hi:[1,0,1]
	v_mov_b32_e32 v170, v243
	v_pk_fma_f32 v[172:173], v[90:91], v[170:171], v[168:169] op_sel_hi:[1,0,1]
	ds_read_b128 v[236:239], v244 offset:9216
	s_waitcnt lgkmcnt(3)
	v_pk_fma_f32 v[172:173], v[76:77], v[224:225], v[172:173] op_sel_hi:[1,0,1]
	s_nop 0
	v_pk_fma_f32 v[168:169], v[78:79], v[224:225], v[172:173] op_sel:[0,1,0]
	s_nop 0
	v_pk_fma_f32 v[168:169], v[84:85], v[226:227], v[168:169] op_sel_hi:[1,0,1]
	v_mov_b32_e32 v170, v227
	v_pk_fma_f32 v[172:173], v[88:89], v[170:171], v[168:169] op_sel_hi:[1,0,1]
	ds_read_b128 v[240:243], v244 offset:10240
	s_waitcnt lgkmcnt(3)
	v_pk_fma_f32 v[172:173], v[68:69], v[228:229], v[172:173] op_sel_hi:[1,0,1]
	s_nop 0
	v_pk_fma_f32 v[168:169], v[70:71], v[228:229], v[172:173] op_sel:[0,1,0]
	s_nop 0
	v_pk_fma_f32 v[168:169], v[72:73], v[230:231], v[168:169] op_sel_hi:[1,0,1]
	v_mov_b32_e32 v170, v231
	v_pk_fma_f32 v[168:169], v[74:75], v[170:171], v[168:169] op_sel_hi:[1,0,1]
	ds_read_b128 v[224:227], v244 offset:11264
	s_waitcnt lgkmcnt(3)
	v_pk_fma_f32 v[174:175], v[124:125], v[232:233], 0 op_sel_hi:[1,0,0]
	s_nop 0
	v_pk_fma_f32 v[170:171], v[126:127], v[232:233], v[174:175] op_sel:[0,1,0]
	s_nop 0
	v_pk_fma_f32 v[170:171], v[128:129], v[234:235], v[170:171] op_sel_hi:[1,0,1]
	v_mov_b32_e32 v172, v235
	v_pk_fma_f32 v[174:175], v[130:131], v[172:173], v[170:171] op_sel_hi:[1,0,1]
	ds_read_b128 v[228:231], v244 offset:12288
	s_waitcnt lgkmcnt(3)
	v_pk_fma_f32 v[174:175], v[112:113], v[236:237], v[174:175] op_sel_hi:[1,0,1]
	s_nop 0
	v_pk_fma_f32 v[170:171], v[114:115], v[236:237], v[174:175] op_sel:[0,1,0]
	s_nop 0
	v_pk_fma_f32 v[170:171], v[118:119], v[238:239], v[170:171] op_sel_hi:[1,0,1]
	v_mov_b32_e32 v172, v239
	v_pk_fma_f32 v[174:175], v[122:123], v[172:173], v[170:171] op_sel_hi:[1,0,1]
	ds_read_b128 v[232:235], v244 offset:13312
	s_waitcnt lgkmcnt(3)
	v_pk_fma_f32 v[174:175], v[108:109], v[240:241], v[174:175] op_sel_hi:[1,0,1]
	s_nop 0
	v_pk_fma_f32 v[170:171], v[110:111], v[240:241], v[174:175] op_sel:[0,1,0]
	s_nop 0
	v_pk_fma_f32 v[170:171], v[116:117], v[242:243], v[170:171] op_sel_hi:[1,0,1]
	v_mov_b32_e32 v172, v243
	v_pk_fma_f32 v[174:175], v[120:121], v[172:173], v[170:171] op_sel_hi:[1,0,1]
	ds_read_b128 v[236:239], v244 offset:14336
	s_waitcnt lgkmcnt(3)
	v_pk_fma_f32 v[174:175], v[96:97], v[224:225], v[174:175] op_sel_hi:[1,0,1]
	s_nop 0
	v_pk_fma_f32 v[170:171], v[98:99], v[224:225], v[174:175] op_sel:[0,1,0]
	s_nop 0
	v_pk_fma_f32 v[170:171], v[102:103], v[226:227], v[170:171] op_sel_hi:[1,0,1]
	v_mov_b32_e32 v172, v227
	v_pk_fma_f32 v[174:175], v[106:107], v[172:173], v[170:171] op_sel_hi:[1,0,1]
	ds_read_b128 v[240:243], v244 offset:15360
	s_waitcnt lgkmcnt(3)
	v_pk_fma_f32 v[174:175], v[92:93], v[228:229], v[174:175] op_sel_hi:[1,0,1]
	s_nop 0
	v_pk_fma_f32 v[170:171], v[94:95], v[228:229], v[174:175] op_sel:[0,1,0]
	s_nop 0
	v_pk_fma_f32 v[170:171], v[100:101], v[230:231], v[170:171] op_sel_hi:[1,0,1]
	v_mov_b32_e32 v172, v231
	v_pk_fma_f32 v[174:175], v[104:105], v[172:173], v[170:171] op_sel_hi:[1,0,1]
	ds_read_b128 v[224:227], v244 offset:16384
	s_waitcnt lgkmcnt(3)
	v_pk_fma_f32 v[174:175], v[80:81], v[232:233], v[174:175] op_sel_hi:[1,0,1]
	s_nop 0
	v_pk_fma_f32 v[170:171], v[82:83], v[232:233], v[174:175] op_sel:[0,1,0]
	s_nop 0
	v_pk_fma_f32 v[170:171], v[86:87], v[234:235], v[170:171] op_sel_hi:[1,0,1]
	v_mov_b32_e32 v172, v235
	v_pk_fma_f32 v[174:175], v[90:91], v[172:173], v[170:171] op_sel_hi:[1,0,1]
	ds_read_b128 v[228:231], v244 offset:17408
	s_waitcnt lgkmcnt(3)
	v_pk_fma_f32 v[174:175], v[76:77], v[236:237], v[174:175] op_sel_hi:[1,0,1]
	s_nop 0
	v_pk_fma_f32 v[170:171], v[78:79], v[236:237], v[174:175] op_sel:[0,1,0]
	s_nop 0
	v_pk_fma_f32 v[170:171], v[84:85], v[238:239], v[170:171] op_sel_hi:[1,0,1]
	v_mov_b32_e32 v172, v239
	v_pk_fma_f32 v[174:175], v[88:89], v[172:173], v[170:171] op_sel_hi:[1,0,1]
	ds_read_b128 v[232:235], v244 offset:18432
	s_waitcnt lgkmcnt(3)
	v_pk_fma_f32 v[174:175], v[68:69], v[240:241], v[174:175] op_sel_hi:[1,0,1]
	s_nop 0
	v_pk_fma_f32 v[170:171], v[70:71], v[240:241], v[174:175] op_sel:[0,1,0]
	s_nop 0
	v_pk_fma_f32 v[170:171], v[72:73], v[242:243], v[170:171] op_sel_hi:[1,0,1]
	v_mov_b32_e32 v172, v243
	v_pk_fma_f32 v[170:171], v[74:75], v[172:173], v[170:171] op_sel_hi:[1,0,1]
	ds_read_b128 v[236:239], v244 offset:19456
	s_waitcnt lgkmcnt(3)
	v_pk_fma_f32 v[176:177], v[124:125], v[224:225], 0 op_sel_hi:[1,0,0]
	s_nop 0
	v_pk_fma_f32 v[172:173], v[126:127], v[224:225], v[176:177] op_sel:[0,1,0]
	s_nop 0
	v_pk_fma_f32 v[172:173], v[128:129], v[226:227], v[172:173] op_sel_hi:[1,0,1]
	v_mov_b32_e32 v174, v227
	v_pk_fma_f32 v[176:177], v[130:131], v[174:175], v[172:173] op_sel_hi:[1,0,1]
	ds_read_b128 v[240:243], v244 offset:20480
	s_waitcnt lgkmcnt(3)
	v_pk_fma_f32 v[176:177], v[112:113], v[228:229], v[176:177] op_sel_hi:[1,0,1]
	s_nop 0
	v_pk_fma_f32 v[172:173], v[114:115], v[228:229], v[176:177] op_sel:[0,1,0]
	s_nop 0
	v_pk_fma_f32 v[172:173], v[118:119], v[230:231], v[172:173] op_sel_hi:[1,0,1]
	v_mov_b32_e32 v174, v231
	v_pk_fma_f32 v[176:177], v[122:123], v[174:175], v[172:173] op_sel_hi:[1,0,1]
	ds_read_b128 v[224:227], v244 offset:21504
	s_waitcnt lgkmcnt(3)
; #define LAS __attribute__((address_space(3)))
; __device__ __forceinline__ void phase_norm2(const Params& p, const Ctx& F, const int l) {
;     ...
; #pragma unroll
;         for (int e = 0; e < 16; ++e) { f32x2 a = {0.f, 0.f};
; #pragma unroll
;             for (int j = 0; j < 8; ++j) { const f32x4 w = *((const LAS f32x4*)(wr2 + e * DM) + F.lane + 64 * j);
; #pragma unroll
;                 for (int c = 0; c < 4; ++c) a += vv[j][c] * w[c]; }
;             lg[e] = a; }
	v_pk_fma_f32 v[176:177], v[108:109], v[232:233], v[176:177] op_sel_hi:[1,0,1]
	s_nop 0
	v_pk_fma_f32 v[172:173], v[110:111], v[232:233], v[176:177] op_sel:[0,1,0]
	s_nop 0
	v_pk_fma_f32 v[172:173], v[116:117], v[234:235], v[172:173] op_sel_hi:[1,0,1]
	v_mov_b32_e32 v174, v235
	v_pk_fma_f32 v[176:177], v[120:121], v[174:175], v[172:173] op_sel_hi:[1,0,1]
	ds_read_b128 v[228:231], v244 offset:22528
	s_waitcnt lgkmcnt(3)
	v_pk_fma_f32 v[176:177], v[96:97], v[236:237], v[176:177] op_sel_hi:[1,0,1]
	s_nop 0
	v_pk_fma_f32 v[172:173], v[98:99], v[236:237], v[176:177] op_sel:[0,1,0]
	s_nop 0
	v_pk_fma_f32 v[172:173], v[102:103], v[238:239], v[172:173] op_sel_hi:[1,0,1]
	v_mov_b32_e32 v174, v239
	v_pk_fma_f32 v[176:177], v[106:107], v[174:175], v[172:173] op_sel_hi:[1,0,1]
	ds_read_b128 v[232:235], v244 offset:23552
	s_waitcnt lgkmcnt(3)
	v_pk_fma_f32 v[176:177], v[92:93], v[240:241], v[176:177] op_sel_hi:[1,0,1]
	s_nop 0
	v_pk_fma_f32 v[172:173], v[94:95], v[240:241], v[176:177] op_sel:[0,1,0]
	s_nop 0
	v_pk_fma_f32 v[172:173], v[100:101], v[242:243], v[172:173] op_sel_hi:[1,0,1]
	v_mov_b32_e32 v174, v243
	v_pk_fma_f32 v[176:177], v[104:105], v[174:175], v[172:173] op_sel_hi:[1,0,1]
	ds_read_b128 v[236:239], v244 offset:24576
	s_waitcnt lgkmcnt(3)
	v_pk_fma_f32 v[176:177], v[80:81], v[224:225], v[176:177] op_sel_hi:[1,0,1]
	s_nop 0
	v_pk_fma_f32 v[172:173], v[82:83], v[224:225], v[176:177] op_sel:[0,1,0]
	s_nop 0
	v_pk_fma_f32 v[172:173], v[86:87], v[226:227], v[172:173] op_sel_hi:[1,0,1]
	v_mov_b32_e32 v174, v227
	v_pk_fma_f32 v[176:177], v[90:91], v[174:175], v[172:173] op_sel_hi:[1,0,1]
	ds_read_b128 v[240:243], v244 offset:25600
	s_waitcnt lgkmcnt(3)
	v_pk_fma_f32 v[176:177], v[76:77], v[228:229], v[176:177] op_sel_hi:[1,0,1]
	s_nop 0
	v_pk_fma_f32 v[172:173], v[78:79], v[228:229], v[176:177] op_sel:[0,1,0]
	s_nop 0
	v_pk_fma_f32 v[172:173], v[84:85], v[230:231], v[172:173] op_sel_hi:[1,0,1]
	v_mov_b32_e32 v174, v231
	v_pk_fma_f32 v[176:177], v[88:89], v[174:175], v[172:173] op_sel_hi:[1,0,1]
	ds_read_b128 v[224:227], v244 offset:26624
	s_waitcnt lgkmcnt(3)
	v_pk_fma_f32 v[176:177], v[68:69], v[232:233], v[176:177] op_sel_hi:[1,0,1]
	s_nop 0
	v_pk_fma_f32 v[172:173], v[70:71], v[232:233], v[176:177] op_sel:[0,1,0]
	s_nop 0
	v_pk_fma_f32 v[172:173], v[72:73], v[234:235], v[172:173] op_sel_hi:[1,0,1]
	v_mov_b32_e32 v174, v235
	v_pk_fma_f32 v[172:173], v[74:75], v[174:175], v[172:173] op_sel_hi:[1,0,1]
	ds_read_b128 v[228:231], v244 offset:27648
	s_waitcnt lgkmcnt(3)
	v_pk_fma_f32 v[178:179], v[124:125], v[236:237], 0 op_sel_hi:[1,0,0]
	s_nop 0
	v_pk_fma_f32 v[174:175], v[126:127], v[236:237], v[178:179] op_sel:[0,1,0]
	s_nop 0
	v_pk_fma_f32 v[174:175], v[128:129], v[238:239], v[174:175] op_sel_hi:[1,0,1]
	v_mov_b32_e32 v176, v239
	v_pk_fma_f32 v[178:179], v[130:131], v[176:177], v[174:175] op_sel_hi:[1,0,1]
	ds_read_b128 v[232:235], v244 offset:28672
	s_waitcnt lgkmcnt(3)
	v_pk_fma_f32 v[178:179], v[112:113], v[240:241], v[178:179] op_sel_hi:[1,0,1]
	s_nop 0
	v_pk_fma_f32 v[174:175], v[114:115], v[240:241], v[178:179] op_sel:[0,1,0]
	s_nop 0
	v_pk_fma_f32 v[174:175], v[118:119], v[242:243], v[174:175] op_sel_hi:[1,0,1]
	v_mov_b32_e32 v176, v243
	v_pk_fma_f32 v[178:179], v[122:123], v[176:177], v[174:175] op_sel_hi:[1,0,1]
	ds_read_b128 v[236:239], v244 offset:29696
	s_waitcnt lgkmcnt(3)
	v_pk_fma_f32 v[178:179], v[108:109], v[224:225], v[178:179] op_sel_hi:[1,0,1]
	s_nop 0
	v_pk_fma_f32 v[174:175], v[110:111], v[224:225], v[178:179] op_sel:[0,1,0]
	s_nop 0
	v_pk_fma_f32 v[174:175], v[116:117], v[226:227], v[174:175] op_sel_hi:[1,0,1]
	v_mov_b32_e32 v176, v227
	v_pk_fma_f32 v[178:179], v[120:121], v[176:177], v[174:175] op_sel_hi:[1,0,1]
	ds_read_b128 v[240:243], v244 offset:30720
	s_waitcnt lgkmcnt(3)
	v_pk_fma_f32 v[178:179], v[96:97], v[228:229], v[178:179] op_sel_hi:[1,0,1]
	s_nop 0
	v_pk_fma_f32 v[174:175], v[98:99], v[228:229], v[178:179] op_sel:[0,1,0]
	s_nop 0
	v_pk_fma_f32 v[174:175], v[102:103], v[230:231], v[174:175] op_sel_hi:[1,0,1]
	v_mov_b32_e32 v176, v231
	v_pk_fma_f32 v[178:179], v[106:107], v[176:177], v[174:175] op_sel_hi:[1,0,1]
	ds_read_b128 v[224:227], v244 offset:31744
	s_waitcnt lgkmcnt(3)
	v_pk_fma_f32 v[178:179], v[92:93], v[232:233], v[178:179] op_sel_hi:[1,0,1]
	s_nop 0
	v_pk_fma_f32 v[174:175], v[94:95], v[232:233], v[178:179] op_sel:[0,1,0]
	s_nop 0
	v_pk_fma_f32 v[174:175], v[100:101], v[234:235], v[174:175] op_sel_hi:[1,0,1]
	v_mov_b32_e32 v176, v235
	v_pk_fma_f32 v[178:179], v[104:105], v[176:177], v[174:175] op_sel_hi:[1,0,1]
	ds_read_b128 v[228:231], v244 offset:32768
	s_waitcnt lgkmcnt(3)
	v_pk_fma_f32 v[178:179], v[80:81], v[236:237], v[178:179] op_sel_hi:[1,0,1]
	s_nop 0
	v_pk_fma_f32 v[174:175], v[82:83], v[236:237], v[178:179] op_sel:[0,1,0]
	s_nop 0
	v_pk_fma_f32 v[174:175], v[86:87], v[238:239], v[174:175] op_sel_hi:[1,0,1]
	v_mov_b32_e32 v176, v239
	v_pk_fma_f32 v[178:179], v[90:91], v[176:177], v[174:175] op_sel_hi:[1,0,1]
	ds_read_b128 v[232:235], v244 offset:33792
	s_waitcnt lgkmcnt(3)
	v_pk_fma_f32 v[178:179], v[76:77], v[240:241], v[178:179] op_sel_hi:[1,0,1]
	s_nop 0
	v_pk_fma_f32 v[174:175], v[78:79], v[240:241], v[178:179] op_sel:[0,1,0]
	s_nop 0
	v_pk_fma_f32 v[174:175], v[84:85], v[242:243], v[174:175] op_sel_hi:[1,0,1]
	v_mov_b32_e32 v176, v243
	v_pk_fma_f32 v[178:179], v[88:89], v[176:177], v[174:175] op_sel_hi:[1,0,1]
	ds_read_b128 v[236:239], v244 offset:34816
	s_waitcnt lgkmcnt(3)
; #define LAS __attribute__((address_space(3)))
; __device__ __forceinline__ void phase_norm2(const Params& p, const Ctx& F, const int l) {
;     ...
; #pragma unroll
;         for (int e = 0; e < 16; ++e) { f32x2 a = {0.f, 0.f};
; #pragma unroll
;             for (int j = 0; j < 8; ++j) { const f32x4 w = *((const LAS f32x4*)(wr2 + e * DM) + F.lane + 64 * j);
; #pragma unroll
;                 for (int c = 0; c < 4; ++c) a += vv[j][c] * w[c]; }
;             lg[e] = a; }
	v_pk_fma_f32 v[178:179], v[68:69], v[224:225], v[178:179] op_sel_hi:[1,0,1]
	s_nop 0
	v_pk_fma_f32 v[174:175], v[70:71], v[224:225], v[178:179] op_sel:[0,1,0]
	s_nop 0
	v_pk_fma_f32 v[174:175], v[72:73], v[226:227], v[174:175] op_sel_hi:[1,0,1]
	v_mov_b32_e32 v176, v227
	v_pk_fma_f32 v[174:175], v[74:75], v[176:177], v[174:175] op_sel_hi:[1,0,1]
	ds_read_b128 v[240:243], v244 offset:35840
	s_waitcnt lgkmcnt(3)
	v_pk_fma_f32 v[180:181], v[124:125], v[228:229], 0 op_sel_hi:[1,0,0]
	s_nop 0
	v_pk_fma_f32 v[176:177], v[126:127], v[228:229], v[180:181] op_sel:[0,1,0]
	s_nop 0
	v_pk_fma_f32 v[176:177], v[128:129], v[230:231], v[176:177] op_sel_hi:[1,0,1]
	v_mov_b32_e32 v178, v231
	v_pk_fma_f32 v[180:181], v[130:131], v[178:179], v[176:177] op_sel_hi:[1,0,1]
	ds_read_b128 v[224:227], v244 offset:36864
	s_waitcnt lgkmcnt(3)
	v_pk_fma_f32 v[180:181], v[112:113], v[232:233], v[180:181] op_sel_hi:[1,0,1]
	s_nop 0
	v_pk_fma_f32 v[176:177], v[114:115], v[232:233], v[180:181] op_sel:[0,1,0]
	s_nop 0
	v_pk_fma_f32 v[176:177], v[118:119], v[234:235], v[176:177] op_sel_hi:[1,0,1]
	v_mov_b32_e32 v178, v235
	v_pk_fma_f32 v[180:181], v[122:123], v[178:179], v[176:177] op_sel_hi:[1,0,1]
	ds_read_b128 v[228:231], v244 offset:37888
	s_waitcnt lgkmcnt(3)
	v_pk_fma_f32 v[180:181], v[108:109], v[236:237], v[180:181] op_sel_hi:[1,0,1]
	s_nop 0
	v_pk_fma_f32 v[176:177], v[110:111], v[236:237], v[180:181] op_sel:[0,1,0]
	s_nop 0
	v_pk_fma_f32 v[176:177], v[116:117], v[238:239], v[176:177] op_sel_hi:[1,0,1]
	v_mov_b32_e32 v178, v239
	v_pk_fma_f32 v[180:181], v[120:121], v[178:179], v[176:177] op_sel_hi:[1,0,1]
	ds_read_b128 v[232:235], v244 offset:38912
	s_waitcnt lgkmcnt(3)
	v_pk_fma_f32 v[180:181], v[96:97], v[240:241], v[180:181] op_sel_hi:[1,0,1]
	s_nop 0
	v_pk_fma_f32 v[176:177], v[98:99], v[240:241], v[180:181] op_sel:[0,1,0]
	s_nop 0
	v_pk_fma_f32 v[176:177], v[102:103], v[242:243], v[176:177] op_sel_hi:[1,0,1]
	v_mov_b32_e32 v178, v243
	v_pk_fma_f32 v[180:181], v[106:107], v[178:179], v[176:177] op_sel_hi:[1,0,1]
	ds_read_b128 v[236:239], v244 offset:39936
	s_waitcnt lgkmcnt(3)
	v_pk_fma_f32 v[180:181], v[92:93], v[224:225], v[180:181] op_sel_hi:[1,0,1]
	s_nop 0
	v_pk_fma_f32 v[176:177], v[94:95], v[224:225], v[180:181] op_sel:[0,1,0]
	s_nop 0
	v_pk_fma_f32 v[176:177], v[100:101], v[226:227], v[176:177] op_sel_hi:[1,0,1]
	v_mov_b32_e32 v178, v227
	v_pk_fma_f32 v[180:181], v[104:105], v[178:179], v[176:177] op_sel_hi:[1,0,1]
	ds_read_b128 v[240:243], v244 offset:40960
	s_waitcnt lgkmcnt(3)
	v_pk_fma_f32 v[180:181], v[80:81], v[228:229], v[180:181] op_sel_hi:[1,0,1]
	s_nop 0
	v_pk_fma_f32 v[176:177], v[82:83], v[228:229], v[180:181] op_sel:[0,1,0]
	s_nop 0
	v_pk_fma_f32 v[176:177], v[86:87], v[230:231], v[176:177] op_sel_hi:[1,0,1]
	v_mov_b32_e32 v178, v231
	v_pk_fma_f32 v[180:181], v[90:91], v[178:179], v[176:177] op_sel_hi:[1,0,1]
	ds_read_b128 v[224:227], v244 offset:41984
	s_waitcnt lgkmcnt(3)
	v_pk_fma_f32 v[180:181], v[76:77], v[232:233], v[180:181] op_sel_hi:[1,0,1]
	s_nop 0
	v_pk_fma_f32 v[176:177], v[78:79], v[232:233], v[180:181] op_sel:[0,1,0]
	s_nop 0
	v_pk_fma_f32 v[176:177], v[84:85], v[234:235], v[176:177] op_sel_hi:[1,0,1]
	v_mov_b32_e32 v178, v235
	v_pk_fma_f32 v[180:181], v[88:89], v[178:179], v[176:177] op_sel_hi:[1,0,1]
	ds_read_b128 v[228:231], v244 offset:43008
	s_waitcnt lgkmcnt(3)
	v_pk_fma_f32 v[180:181], v[68:69], v[236:237], v[180:181] op_sel_hi:[1,0,1]
	s_nop 0
	v_pk_fma_f32 v[176:177], v[70:71], v[236:237], v[180:181] op_sel:[0,1,0]
	s_nop 0
	v_pk_fma_f32 v[176:177], v[72:73], v[238:239], v[176:177] op_sel_hi:[1,0,1]
	v_mov_b32_e32 v178, v239
	v_pk_fma_f32 v[176:177], v[74:75], v[178:179], v[176:177] op_sel_hi:[1,0,1]
	ds_read_b128 v[232:235], v244 offset:44032
	s_waitcnt lgkmcnt(3)
	v_pk_fma_f32 v[184:185], v[124:125], v[240:241], 0 op_sel_hi:[1,0,0]
	s_nop 0
	v_pk_fma_f32 v[178:179], v[126:127], v[240:241], v[184:185] op_sel:[0,1,0]
	s_nop 0
	v_pk_fma_f32 v[178:179], v[128:129], v[242:243], v[178:179] op_sel_hi:[1,0,1]
	v_mov_b32_e32 v180, v243
	v_pk_fma_f32 v[184:185], v[130:131], v[180:181], v[178:179] op_sel_hi:[1,0,1]
	ds_read_b128 v[236:239], v244 offset:45056
	s_waitcnt lgkmcnt(3)
	v_pk_fma_f32 v[184:185], v[112:113], v[224:225], v[184:185] op_sel_hi:[1,0,1]
	s_nop 0
	v_pk_fma_f32 v[178:179], v[114:115], v[224:225], v[184:185] op_sel:[0,1,0]
	s_nop 0
	v_pk_fma_f32 v[178:179], v[118:119], v[226:227], v[178:179] op_sel_hi:[1,0,1]
	v_mov_b32_e32 v180, v227
	v_pk_fma_f32 v[184:185], v[122:123], v[180:181], v[178:179] op_sel_hi:[1,0,1]
	ds_read_b128 v[240:243], v244 offset:46080
	s_waitcnt lgkmcnt(3)
	v_pk_fma_f32 v[184:185], v[108:109], v[228:229], v[184:185] op_sel_hi:[1,0,1]
	s_nop 0
	v_pk_fma_f32 v[178:179], v[110:111], v[228:229], v[184:185] op_sel:[0,1,0]
	s_nop 0
	v_pk_fma_f32 v[178:179], v[116:117], v[230:231], v[178:179] op_sel_hi:[1,0,1]
	v_mov_b32_e32 v180, v231
	v_pk_fma_f32 v[184:185], v[120:121], v[180:181], v[178:179] op_sel_hi:[1,0,1]
	ds_read_b128 v[224:227], v244 offset:47104
	s_waitcnt lgkmcnt(3)
	v_pk_fma_f32 v[184:185], v[96:97], v[232:233], v[184:185] op_sel_hi:[1,0,1]
	s_nop 0
	v_pk_fma_f32 v[178:179], v[98:99], v[232:233], v[184:185] op_sel:[0,1,0]
	s_nop 0
	v_pk_fma_f32 v[178:179], v[102:103], v[234:235], v[178:179] op_sel_hi:[1,0,1]
	v_mov_b32_e32 v180, v235
	v_pk_fma_f32 v[184:185], v[106:107], v[180:181], v[178:179] op_sel_hi:[1,0,1]
	ds_read_b128 v[228:231], v244 offset:48128
	s_waitcnt lgkmcnt(3)
; #define LAS __attribute__((address_space(3)))
; __device__ __forceinline__ void phase_norm2(const Params& p, const Ctx& F, const int l) {
;     ...
; #pragma unroll
;         for (int e = 0; e < 16; ++e) { f32x2 a = {0.f, 0.f};
; #pragma unroll
;             for (int j = 0; j < 8; ++j) { const f32x4 w = *((const LAS f32x4*)(wr2 + e * DM) + F.lane + 64 * j);
; #pragma unroll
;                 for (int c = 0; c < 4; ++c) a += vv[j][c] * w[c]; }
;             lg[e] = a; }
	v_pk_fma_f32 v[184:185], v[92:93], v[236:237], v[184:185] op_sel_hi:[1,0,1]
	s_nop 0
	v_pk_fma_f32 v[178:179], v[94:95], v[236:237], v[184:185] op_sel:[0,1,0]
	s_nop 0
	v_pk_fma_f32 v[178:179], v[100:101], v[238:239], v[178:179] op_sel_hi:[1,0,1]
	v_mov_b32_e32 v180, v239
	v_pk_fma_f32 v[184:185], v[104:105], v[180:181], v[178:179] op_sel_hi:[1,0,1]
	ds_read_b128 v[232:235], v244 offset:49152
	s_waitcnt lgkmcnt(3)
	v_pk_fma_f32 v[184:185], v[80:81], v[240:241], v[184:185] op_sel_hi:[1,0,1]
	s_nop 0
	v_pk_fma_f32 v[178:179], v[82:83], v[240:241], v[184:185] op_sel:[0,1,0]
	s_nop 0
	v_pk_fma_f32 v[178:179], v[86:87], v[242:243], v[178:179] op_sel_hi:[1,0,1]
	v_mov_b32_e32 v180, v243
	v_pk_fma_f32 v[184:185], v[90:91], v[180:181], v[178:179] op_sel_hi:[1,0,1]
	ds_read_b128 v[236:239], v244 offset:50176
	s_waitcnt lgkmcnt(3)
	v_pk_fma_f32 v[184:185], v[76:77], v[224:225], v[184:185] op_sel_hi:[1,0,1]
	s_nop 0
	v_pk_fma_f32 v[178:179], v[78:79], v[224:225], v[184:185] op_sel:[0,1,0]
	s_nop 0
	v_pk_fma_f32 v[178:179], v[84:85], v[226:227], v[178:179] op_sel_hi:[1,0,1]
	v_mov_b32_e32 v180, v227
	v_pk_fma_f32 v[184:185], v[88:89], v[180:181], v[178:179] op_sel_hi:[1,0,1]
	ds_read_b128 v[240:243], v244 offset:51200
	s_waitcnt lgkmcnt(3)
	v_pk_fma_f32 v[184:185], v[68:69], v[228:229], v[184:185] op_sel_hi:[1,0,1]
	s_nop 0
	v_pk_fma_f32 v[178:179], v[70:71], v[228:229], v[184:185] op_sel:[0,1,0]
	ds_read_b128 v[224:227], v244 offset:52224
	v_pk_fma_f32 v[178:179], v[72:73], v[230:231], v[178:179] op_sel_hi:[1,0,1]
	v_mov_b32_e32 v180, v231
	v_pk_fma_f32 v[178:179], v[74:75], v[180:181], v[178:179] op_sel_hi:[1,0,1]
	s_waitcnt lgkmcnt(3)
	v_pk_fma_f32 v[180:181], v[124:125], v[232:233], 0 op_sel_hi:[1,0,0]
	s_nop 0
	v_pk_fma_f32 v[180:181], v[126:127], v[232:233], v[180:181] op_sel:[0,1,0]
	v_mov_b32_e32 v184, v235
	v_pk_fma_f32 v[180:181], v[128:129], v[234:235], v[180:181] op_sel_hi:[1,0,1]
	s_nop 0
	v_pk_fma_f32 v[180:181], v[130:131], v[184:185], v[180:181] op_sel_hi:[1,0,1]
	ds_read_b128 v[228:231], v244 offset:53248
	s_waitcnt lgkmcnt(3)
	v_pk_fma_f32 v[180:181], v[112:113], v[236:237], v[180:181] op_sel_hi:[1,0,1]
	s_nop 0
	v_pk_fma_f32 v[180:181], v[114:115], v[236:237], v[180:181] op_sel:[0,1,0]
	v_mov_b32_e32 v184, v239
	v_pk_fma_f32 v[180:181], v[118:119], v[238:239], v[180:181] op_sel_hi:[1,0,1]
	s_nop 0
	v_pk_fma_f32 v[180:181], v[122:123], v[184:185], v[180:181] op_sel_hi:[1,0,1]
	ds_read_b128 v[232:235], v244 offset:54272
	s_waitcnt lgkmcnt(3)
	v_pk_fma_f32 v[180:181], v[108:109], v[240:241], v[180:181] op_sel_hi:[1,0,1]
	s_nop 0
	v_pk_fma_f32 v[180:181], v[110:111], v[240:241], v[180:181] op_sel:[0,1,0]
	v_mov_b32_e32 v184, v243
	v_pk_fma_f32 v[180:181], v[116:117], v[242:243], v[180:181] op_sel_hi:[1,0,1]
	s_nop 0
	v_pk_fma_f32 v[180:181], v[120:121], v[184:185], v[180:181] op_sel_hi:[1,0,1]
	ds_read_b128 v[236:239], v244 offset:55296
	s_waitcnt lgkmcnt(3)
	v_pk_fma_f32 v[180:181], v[96:97], v[224:225], v[180:181] op_sel_hi:[1,0,1]
	s_nop 0
	v_pk_fma_f32 v[180:181], v[98:99], v[224:225], v[180:181] op_sel:[0,1,0]
	v_mov_b32_e32 v184, v227
	v_pk_fma_f32 v[180:181], v[102:103], v[226:227], v[180:181] op_sel_hi:[1,0,1]
	s_nop 0
	v_pk_fma_f32 v[180:181], v[106:107], v[184:185], v[180:181] op_sel_hi:[1,0,1]
	ds_read_b128 v[240:243], v244 offset:56320
	s_waitcnt lgkmcnt(3)
	v_pk_fma_f32 v[180:181], v[92:93], v[228:229], v[180:181] op_sel_hi:[1,0,1]
	s_nop 0
	v_pk_fma_f32 v[180:181], v[94:95], v[228:229], v[180:181] op_sel:[0,1,0]
	v_mov_b32_e32 v184, v231
	v_pk_fma_f32 v[180:181], v[100:101], v[230:231], v[180:181] op_sel_hi:[1,0,1]
	s_nop 0
	v_pk_fma_f32 v[180:181], v[104:105], v[184:185], v[180:181] op_sel_hi:[1,0,1]
	ds_read_b128 v[224:227], v244 offset:57344
	s_waitcnt lgkmcnt(3)
	v_pk_fma_f32 v[180:181], v[80:81], v[232:233], v[180:181] op_sel_hi:[1,0,1]
	s_nop 0
	v_pk_fma_f32 v[180:181], v[82:83], v[232:233], v[180:181] op_sel:[0,1,0]
	v_mov_b32_e32 v184, v235
	v_pk_fma_f32 v[180:181], v[86:87], v[234:235], v[180:181] op_sel_hi:[1,0,1]
	s_nop 0
	v_pk_fma_f32 v[180:181], v[90:91], v[184:185], v[180:181] op_sel_hi:[1,0,1]
	ds_read_b128 v[228:231], v244 offset:58368
	s_waitcnt lgkmcnt(3)
	v_pk_fma_f32 v[180:181], v[76:77], v[236:237], v[180:181] op_sel_hi:[1,0,1]
	s_nop 0
	v_pk_fma_f32 v[180:181], v[78:79], v[236:237], v[180:181] op_sel:[0,1,0]
	v_mov_b32_e32 v184, v239
	v_pk_fma_f32 v[180:181], v[84:85], v[238:239], v[180:181] op_sel_hi:[1,0,1]
	s_nop 0
	v_pk_fma_f32 v[180:181], v[88:89], v[184:185], v[180:181] op_sel_hi:[1,0,1]
	ds_read_b128 v[232:235], v244 offset:59392
	s_waitcnt lgkmcnt(3)
	v_pk_fma_f32 v[180:181], v[68:69], v[240:241], v[180:181] op_sel_hi:[1,0,1]
	s_nop 0
	v_pk_fma_f32 v[180:181], v[70:71], v[240:241], v[180:181] op_sel:[0,1,0]
	v_mov_b32_e32 v184, v243
	v_pk_fma_f32 v[180:181], v[72:73], v[242:243], v[180:181] op_sel_hi:[1,0,1]
	s_nop 0
	v_pk_fma_f32 v[180:181], v[74:75], v[184:185], v[180:181] op_sel_hi:[1,0,1]
	ds_read_b128 v[236:239], v244 offset:60416
	s_waitcnt lgkmcnt(3)
	v_pk_fma_f32 v[124:125], v[124:125], v[224:225], 0 op_sel_hi:[1,0,0]
	s_nop 0
	v_pk_fma_f32 v[124:125], v[126:127], v[224:225], v[124:125] op_sel:[0,1,0]
	v_mov_b32_e32 v126, v227
	v_pk_fma_f32 v[124:125], v[128:129], v[226:227], v[124:125] op_sel_hi:[1,0,1]
	s_nop 0
	v_pk_fma_f32 v[128:129], v[130:131], v[126:127], v[124:125] op_sel_hi:[1,0,1]
	ds_read_b128 v[240:243], v244 offset:61440
	s_waitcnt lgkmcnt(3)
	v_pk_fma_f32 v[112:113], v[112:113], v[228:229], v[128:129] op_sel_hi:[1,0,1]
	s_nop 0
	v_pk_fma_f32 v[112:113], v[114:115], v[228:229], v[112:113] op_sel:[0,1,0]
	v_mov_b32_e32 v114, v231
	v_pk_fma_f32 v[112:113], v[118:119], v[230:231], v[112:113] op_sel_hi:[1,0,1]
	s_nop 0
	v_pk_fma_f32 v[118:119], v[122:123], v[114:115], v[112:113] op_sel_hi:[1,0,1]
	ds_read_b128 v[224:227], v244 offset:62464
	s_waitcnt lgkmcnt(3)
; #define LAS __attribute__((address_space(3)))
; __device__ __forceinline__ void router_tail(const Ctx& F, const float (&lg)[16], const int b, const int t, const bool valid) {
;     const bool b5 = (F.lane & 32) != 0, b4 = (F.lane & 16) != 0, b3 = (F.lane & 8) != 0, b2 = (F.lane & 4) != 0;
;     float r8[8], r4[4], r2[2];
; #pragma unroll
;     for (int e = 0; e < 8; ++e) { const float keep = b5 ? lg[e + 8] : lg[e], send = b5 ? lg[e] : lg[e + 8]; r8[e] = keep + __shfl_xor(send, 32); }
; #pragma unroll
;     for (int e = 0; e < 4; ++e) { const float keep = b4 ? r8[e + 4] : r8[e], send = b4 ? r8[e] : r8[e + 4]; r4[e] = keep + __shfl_xor(send, 16); }
; #pragma unroll
;     for (int e = 0; e < 2; ++e) { const float keep = b3 ? r4[e + 2] : r4[e], send = b3 ? r4[e] : r4[e + 2]; r2[e] = keep + __shfl_xor(send, 8); }
;     float lgt; { const float keep = b2 ? r2[1] : r2[0], send = b2 ? r2[0] : r2[1]; lgt = keep + __shfl_xor(send, 4); }
;     lgt += __shfl_xor(lgt, 2); lgt += __shfl_xor(lgt, 1);
;     float mx = lgt;
;     mx = fmaxf(mx, __shfl_xor(mx, 4)); mx = fmaxf(mx, __shfl_xor(mx, 8)); mx = fmaxf(mx, __shfl_xor(mx, 16)); mx = fmaxf(mx, __shfl_xor(mx, 32));
;     const float ex = expf(lgt - mx); float sum = ex;
;     sum += __shfl_xor(sum, 4); sum += __shfl_xor(sum, 8); sum += __shfl_xor(sum, 16); sum += __shfl_xor(sum, 32);
;     if (valid && (F.lane & 3) == 0) { const float af = ex / sum; const int e = F.lane >> 2;
;         if (t < CTXL) F.affc[((size_t)(b * 16 + e)) * CTXL + t] = af; else F.affl[((size_t)(b * 16 + e)) * SEQ + (t - CTXL)] = af; }
; __device__ __forceinline__ void phase_norm2(const Params& p, const Ctx& F, const int l) {
;     ...
; #pragma unroll
;         for (int e = 0; e < 16; ++e) { f32x2 a = {0.f, 0.f};
; #pragma unroll
;             for (int j = 0; j < 8; ++j) { const f32x4 w = *((const LAS f32x4*)(wr2 + e * DM) + F.lane + 64 * j);
; #pragma unroll
;                 for (int c = 0; c < 4; ++c) a += vv[j][c] * w[c]; }
;             lg[e] = a; }
	v_pk_fma_f32 v[108:109], v[108:109], v[232:233], v[118:119] op_sel_hi:[1,0,1]
	s_nop 0
	v_pk_fma_f32 v[108:109], v[110:111], v[232:233], v[108:109] op_sel:[0,1,0]
	v_mov_b32_e32 v110, v235
	v_pk_fma_f32 v[108:109], v[116:117], v[234:235], v[108:109] op_sel_hi:[1,0,1]
	s_nop 0
	v_pk_fma_f32 v[112:113], v[120:121], v[110:111], v[108:109] op_sel_hi:[1,0,1]
	ds_read_b128 v[228:231], v244 offset:63488
	s_waitcnt lgkmcnt(3)
	v_pk_fma_f32 v[96:97], v[96:97], v[236:237], v[112:113] op_sel_hi:[1,0,1]
	s_nop 0
	v_pk_fma_f32 v[96:97], v[98:99], v[236:237], v[96:97] op_sel:[0,1,0]
	v_mov_b32_e32 v98, v239
	v_pk_fma_f32 v[96:97], v[102:103], v[238:239], v[96:97] op_sel_hi:[1,0,1]
	s_nop 0
	v_pk_fma_f32 v[102:103], v[106:107], v[98:99], v[96:97] op_sel_hi:[1,0,1]
	ds_read_b128 v[232:235], v244 offset:64512
	s_waitcnt lgkmcnt(3)
	v_pk_fma_f32 v[92:93], v[92:93], v[240:241], v[102:103] op_sel_hi:[1,0,1]
	s_nop 0
	v_pk_fma_f32 v[92:93], v[94:95], v[240:241], v[92:93] op_sel:[0,1,0]
	v_mov_b32_e32 v94, v243
	v_pk_fma_f32 v[92:93], v[100:101], v[242:243], v[92:93] op_sel_hi:[1,0,1]
	s_nop 0
	v_pk_fma_f32 v[96:97], v[104:105], v[94:95], v[92:93] op_sel_hi:[1,0,1]
	s_waitcnt lgkmcnt(2)
	v_pk_fma_f32 v[80:81], v[80:81], v[224:225], v[96:97] op_sel_hi:[1,0,1]
	s_nop 0
	v_pk_fma_f32 v[80:81], v[82:83], v[224:225], v[80:81] op_sel:[0,1,0]
	v_mov_b32_e32 v82, v227
	v_pk_fma_f32 v[80:81], v[86:87], v[226:227], v[80:81] op_sel_hi:[1,0,1]
	s_nop 0
	v_pk_fma_f32 v[86:87], v[90:91], v[82:83], v[80:81] op_sel_hi:[1,0,1]
	s_waitcnt lgkmcnt(1)
	v_pk_fma_f32 v[76:77], v[76:77], v[228:229], v[86:87] op_sel_hi:[1,0,1]
	s_nop 0
	v_pk_fma_f32 v[76:77], v[78:79], v[228:229], v[76:77] op_sel:[0,1,0]
	v_mov_b32_e32 v78, v231
	v_pk_fma_f32 v[76:77], v[84:85], v[230:231], v[76:77] op_sel_hi:[1,0,1]
	s_nop 0
	v_pk_fma_f32 v[80:81], v[88:89], v[78:79], v[76:77] op_sel_hi:[1,0,1]
	v_cndmask_b32_e64 v1, v168, v152, s[38:39]
	s_waitcnt lgkmcnt(0)
	v_pk_fma_f32 v[68:69], v[68:69], v[232:233], v[80:81] op_sel_hi:[1,0,1]
	s_nop 0
	v_pk_fma_f32 v[68:69], v[70:71], v[232:233], v[68:69] op_sel:[0,1,0]
	v_mov_b32_e32 v70, v235
	v_pk_fma_f32 v[68:69], v[72:73], v[234:235], v[68:69] op_sel_hi:[1,0,1]
	v_cndmask_b32_e64 v72, v156, v172, s[38:39]
	v_pk_fma_f32 v[68:69], v[74:75], v[70:71], v[68:69] op_sel_hi:[1,0,1]
	s_nop 1
	v_permlane32_swap_b32_e32 v152, v168
	v_permlane32_swap_b32_e32 v154, v170
	v_permlane32_swap_b32_e32 v156, v172
	v_permlane32_swap_b32_e32 v158, v174
	v_permlane32_swap_b32_e32 v160, v176
	v_permlane32_swap_b32_e32 v162, v178
	v_permlane32_swap_b32_e32 v164, v180
	v_permlane32_swap_b32_e32 v166, v68
	v_add_f32_e32 v1, v152, v168
	v_add_f32_e32 v70, v154, v170
	v_add_f32_e32 v71, v156, v172
	v_add_f32_e32 v72, v158, v174
	v_add_f32_e32 v73, v160, v176
	v_add_f32_e32 v74, v162, v178
	v_add_f32_e32 v75, v164, v180
	v_add_f32_e32 v68, v166, v68
	s_waitcnt lgkmcnt(0)
	s_nop 1
	v_permlane16_swap_b32_e32 v1, v73
	v_permlane16_swap_b32_e32 v70, v74
	v_permlane16_swap_b32_e32 v71, v75
	v_permlane16_swap_b32_e32 v72, v68
	v_add_f32_e32 v1, v1, v73
	v_add_f32_e32 v70, v70, v74
	v_add_f32_e32 v71, v71, v75
	v_add_f32_e32 v68, v72, v68
	v_cndmask_b32_e64 v72, v71, v1, s[42:43]
	v_cndmask_b32_e64 v1, v1, v71, s[42:43]
	v_cndmask_b32_e64 v71, v68, v70, s[42:43]
	v_cndmask_b32_e64 v68, v70, v68, s[42:43]
	s_nop 1
	v_add_f32_dpp v1, v1, v72 row_ror:8 row_mask:0xf bank_mask:0xf
	v_add_f32_dpp v68, v68, v71 row_ror:8 row_mask:0xf bank_mask:0xf
	v_cndmask_b32_e64 v70, v68, v1, s[4:5]
	v_cndmask_b32_e64 v1, v1, v68, s[4:5]
	s_nop 1
	v_mov_b32_dpp v71, v1 row_shl:4 row_mask:0xf bank_mask:0x5
	v_mov_b32_dpp v71, v1 row_shr:4 row_mask:0xf bank_mask:0xa
	v_add_f32_e32 v1, v70, v71
	s_nop 1
	v_add_f32_dpp v1, v1, v1 quad_perm:[2,3,0,1] row_mask:0xf bank_mask:0xf
	s_nop 1
	v_add_f32_dpp v1, v1, v1 quad_perm:[1,0,3,2] row_mask:0xf bank_mask:0xf
	s_nop 1
	v_max_f32_dpp v68, v1, v1 row_half_mirror row_mask:0xf bank_mask:0xf
	s_nop 1
	v_max_f32_dpp v68, v68, v68 row_mirror row_mask:0xf bank_mask:0xf
	v_mov_b32_e32 v70, v68
	s_nop 1
	v_permlane16_swap_b32_e32 v68, v70
	v_max_f32_e32 v68, v68, v70
	v_mov_b32_e32 v70, v68
	s_nop 1
	v_permlane32_swap_b32_e32 v68, v70
	v_max_f32_e32 v68, v68, v70
	v_sub_f32_e32 v1, v1, v68
	v_mul_f32_e32 v68, 0x3fb8aa3b, v1
	v_fma_f32 v70, v1, s55, -v68
	v_rndne_f32_e32 v71, v68
	v_fmac_f32_e32 v70, 0x32a5705f, v1
	v_sub_f32_e32 v68, v68, v71
	v_add_f32_e32 v68, v68, v70
	v_exp_f32_e32 v68, v68
	v_cvt_i32_f32_e32 v70, v71
	v_cmp_ngt_f32_e32 vcc, s56, v1
	v_ldexp_f32 v68, v68, v70
	s_nop 0
	v_cndmask_b32_e32 v68, 0, v68, vcc
	v_cmp_nlt_f32_e32 vcc, s57, v1
	s_nop 1
	v_cndmask_b32_e32 v68, v222, v68, vcc
	s_nop 1
	v_add_f32_dpp v1, v68, v68 row_half_mirror row_mask:0xf bank_mask:0xf
	s_nop 1
	v_add_f32_dpp v1, v1, v1 row_mirror row_mask:0xf bank_mask:0xf
	v_mov_b32_e32 v70, v1
	s_nop 1
	v_permlane16_swap_b32_e32 v1, v70
	v_add_f32_e32 v70, v1, v70
	ds_bpermute_b32 v71, v194, v70
	s_and_saveexec_b64 s[0:1], s[6:7]
	s_cbranch_execz .LBB0_942
	s_waitcnt lgkmcnt(0)
	v_add_f32_e32 v1, v70, v71
	v_div_scale_f32 v70, s[12:13], v1, v1, v68
	v_rcp_f32_e32 v71, v70
	v_div_scale_f32 v72, vcc, v68, v1, v68
	s_cmpk_gt_i32 s60, 0xff
	v_fma_f32 v73, -v70, v71, 1.0
	v_fmac_f32_e32 v71, v73, v71
	v_mul_f32_e32 v73, v72, v71
	v_fma_f32 v74, -v70, v73, v72
	v_fmac_f32_e32 v73, v74, v71
	v_fma_f32 v70, -v70, v73, v72
	v_div_fmas_f32 v70, v70, v71, v73
	v_div_fixup_f32 v68, v70, v1, v68
	s_mov_b64 s[12:13], -1
	s_cbranch_scc0 .LBB0_940
	v_lshl_add_u64 v[70:71], s[60:61], 2, v[148:149]
	global_store_dword v[70:71], v68, off offset:-1024
	s_mov_b64 s[12:13], 0

; __device__ __forceinline__ void router_tail(const Ctx& F, const float (&lg)[16], const int b, const int t, const bool valid) {
;     const bool b5 = (F.lane & 32) != 0, b4 = (F.lane & 16) != 0, b3 = (F.lane & 8) != 0, b2 = (F.lane & 4) != 0;
;     float r8[8], r4[4], r2[2];
; #pragma unroll
;     for (int e = 0; e < 8; ++e) { const float keep = b5 ? lg[e + 8] : lg[e], send = b5 ? lg[e] : lg[e + 8]; r8[e] = keep + __shfl_xor(send, 32); }
; #pragma unroll
;     for (int e = 0; e < 4; ++e) { const float keep = b4 ? r8[e + 4] : r8[e], send = b4 ? r8[e] : r8[e + 4]; r4[e] = keep + __shfl_xor(send, 16); }
; #pragma unroll
;     for (int e = 0; e < 2; ++e) { const float keep = b3 ? r4[e + 2] : r4[e], send = b3 ? r4[e] : r4[e + 2]; r2[e] = keep + __shfl_xor(send, 8); }
;     float lgt; { const float keep = b2 ? r2[1] : r2[0], send = b2 ? r2[0] : r2[1]; lgt = keep + __shfl_xor(send, 4); }
;     lgt += __shfl_xor(lgt, 2); lgt += __shfl_xor(lgt, 1);
;     float mx = lgt;
;     mx = fmaxf(mx, __shfl_xor(mx, 4)); mx = fmaxf(mx, __shfl_xor(mx, 8)); mx = fmaxf(mx, __shfl_xor(mx, 16)); mx = fmaxf(mx, __shfl_xor(mx, 32));
;     const float ex = expf(lgt - mx); float sum = ex;
;     sum += __shfl_xor(sum, 4); sum += __shfl_xor(sum, 8); sum += __shfl_xor(sum, 16); sum += __shfl_xor(sum, 32);
;     if (valid && (F.lane & 3) == 0) { const float af = ex / sum; const int e = F.lane >> 2;
;         if (t < CTXL) F.affc[((size_t)(b * 16 + e)) * CTXL + t] = af; else F.affl[((size_t)(b * 16 + e)) * SEQ + (t - CTXL)] = af; }
.LBB0_942:
	s_or_b64 exec, exec, s[0:1]
	s_and_b64 s[8:9], s[6:7], s[8:9]
	s_waitcnt lgkmcnt(0)
	s_nop 1
	v_permlane32_swap_b32_e32 v153, v169
	v_permlane32_swap_b32_e32 v155, v171
	v_permlane32_swap_b32_e32 v157, v173
	v_permlane32_swap_b32_e32 v159, v175
	v_permlane32_swap_b32_e32 v161, v177
	v_permlane32_swap_b32_e32 v163, v179
	v_permlane32_swap_b32_e32 v165, v181
	v_permlane32_swap_b32_e32 v167, v69
	v_add_f32_e32 v1, v153, v169
	v_add_f32_e32 v68, v155, v171
	v_add_f32_e32 v70, v157, v173
	v_add_f32_e32 v71, v159, v175
	v_add_f32_e32 v72, v161, v177
	v_add_f32_e32 v73, v163, v179
	v_add_f32_e32 v74, v165, v181
	v_add_f32_e32 v69, v167, v69
	s_waitcnt lgkmcnt(0)
	s_nop 1
	v_permlane16_swap_b32_e32 v1, v72
	v_permlane16_swap_b32_e32 v68, v73
	v_permlane16_swap_b32_e32 v70, v74
	v_permlane16_swap_b32_e32 v71, v69
	v_add_f32_e32 v1, v1, v72
	v_add_f32_e32 v68, v68, v73
	v_add_f32_e32 v70, v70, v74
	v_add_f32_e32 v69, v71, v69
	v_cndmask_b32_e64 v71, v70, v1, s[42:43]
	v_cndmask_b32_e64 v1, v1, v70, s[42:43]
	v_cndmask_b32_e64 v70, v69, v68, s[42:43]
	v_cndmask_b32_e64 v68, v68, v69, s[42:43]
	s_nop 1
	v_add_f32_dpp v1, v1, v71 row_ror:8 row_mask:0xf bank_mask:0xf
	v_add_f32_dpp v68, v68, v70 row_ror:8 row_mask:0xf bank_mask:0xf
	v_cndmask_b32_e64 v69, v68, v1, s[4:5]
	v_cndmask_b32_e64 v1, v1, v68, s[4:5]
	s_nop 1
	v_mov_b32_dpp v70, v1 row_shl:4 row_mask:0xf bank_mask:0x5
	v_mov_b32_dpp v70, v1 row_shr:4 row_mask:0xf bank_mask:0xa
	v_add_f32_e32 v1, v69, v70
	s_nop 1
	v_add_f32_dpp v1, v1, v1 quad_perm:[2,3,0,1] row_mask:0xf bank_mask:0xf
	s_nop 1
	v_add_f32_dpp v1, v1, v1 quad_perm:[1,0,3,2] row_mask:0xf bank_mask:0xf
	s_nop 1
	v_max_f32_dpp v68, v1, v1 row_half_mirror row_mask:0xf bank_mask:0xf
	s_nop 1
	v_max_f32_dpp v68, v68, v68 row_mirror row_mask:0xf bank_mask:0xf
	v_mov_b32_e32 v69, v68
	s_nop 1
	v_permlane16_swap_b32_e32 v68, v69
	v_max_f32_e32 v68, v68, v69
	v_mov_b32_e32 v69, v68
	s_nop 1
	v_permlane32_swap_b32_e32 v68, v69
	v_max_f32_e32 v68, v68, v69
	v_sub_f32_e32 v1, v1, v68
	v_mul_f32_e32 v68, 0x3fb8aa3b, v1
	v_fma_f32 v69, v1, s55, -v68
	v_rndne_f32_e32 v70, v68
	v_fmac_f32_e32 v69, 0x32a5705f, v1
	v_sub_f32_e32 v68, v68, v70
	v_add_f32_e32 v68, v68, v69
	v_exp_f32_e32 v68, v68
	v_cvt_i32_f32_e32 v69, v70
	v_cmp_ngt_f32_e32 vcc, s56, v1
	v_ldexp_f32 v68, v68, v69
	s_nop 0
	v_cndmask_b32_e32 v68, 0, v68, vcc
	v_cmp_nlt_f32_e32 vcc, s57, v1
	s_nop 1
	v_cndmask_b32_e32 v68, v222, v68, vcc
	s_nop 1
	v_add_f32_dpp v1, v68, v68 row_half_mirror row_mask:0xf bank_mask:0xf
	s_nop 1
	v_add_f32_dpp v1, v1, v1 row_mirror row_mask:0xf bank_mask:0xf
	v_mov_b32_e32 v69, v1
	s_nop 1
	v_permlane16_swap_b32_e32 v1, v69
	v_add_f32_e32 v69, v1, v69
	ds_bpermute_b32 v70, v194, v69
	s_and_saveexec_b64 s[0:1], s[8:9]
	s_cbranch_execz .LBB0_911
	s_waitcnt lgkmcnt(0)
	v_add_f32_e32 v1, v69, v70
	v_div_scale_f32 v69, s[8:9], v1, v1, v68
	v_rcp_f32_e32 v70, v69
	v_div_scale_f32 v71, vcc, v68, v1, v68
	s_cmpk_gt_i32 s2, 0xff
	v_fma_f32 v72, -v69, v70, 1.0
	v_fmac_f32_e32 v70, v72, v70
	v_mul_f32_e32 v72, v71, v70
	v_fma_f32 v73, -v69, v72, v71
	v_fmac_f32_e32 v72, v73, v70
	v_fma_f32 v69, -v69, v72, v71
	v_div_fmas_f32 v69, v69, v70, v72
	v_div_fixup_f32 v68, v69, v1, v68
	s_mov_b64 s[8:9], -1
	s_cbranch_scc0 .LBB0_945
	s_mov_b32 s3, s61
	v_lshl_add_u64 v[70:71], s[2:3], 2, v[148:149]
	global_store_dword v[70:71], v68, off offset:-1024
	s_mov_b64 s[8:9], 0
